# MoE up GEMM K-loop only: the two LDS-DMA staging loads of phases 2-8 issued inside the MFMA cluster instead of the load segment, counted waits vmcnt(4) (baseline otherwise)
# baseline (speedup 1.0000x reference)
.LBB0_804:
	s_bfe_u32 s0, s66, 0x20001
	s_bfe_u32 s1, s78, 0x10007
	s_lshl_b32 s12, s1, 8
	s_lshl_b32 s44, s0, 9
	s_or_b32 s48, s44, s12
	s_mulk_i32 s0, 0x180
	s_mul_i32 s12, s1, 0xc0
	s_add_i32 s0, s0, s12
	s_lshl_b32 s50, s0, 1
	s_ashr_i32 s0, s78, 4
	s_lshl_b32 s12, s78, 1
	s_and_b32 s0, s0, -16
	s_and_b32 s44, s12, 8
	s_bfe_u32 s80, s78, 0x40003
	s_or_b32 s0, s0, s44
	s_xor_b32 s49, s80, 31
	s_ashr_i32 s0, s0, 3
	s_and_b32 s12, s12, 6
	s_lshl_b32 s83, s49, 8
	s_or_b32 s46, s12, s1
	s_ashr_i32 s1, s0, 31
	s_add_i32 s84, s83, s63
	s_lshr_b32 s81, s78, 3
	v_mov_b32_e32 v172, v1
	s_lshl_b64 s[52:53], s[0:1], 13
	s_ashr_i32 s12, s84, 31
	s_add_u32 s54, s52, s84
	v_and_b32_e32 v168, 31, v172
	v_or_b32_e32 v38, s54, v168
	s_addc_u32 s55, s53, s12
	v_mad_u64_u32 v[2:3], s[44:45], v38, s68, v[146:147]
	s_mul_i32 s82, s46, 0xc0
	v_bfe_u32 v173, v172, 5, 1
	v_mad_i32_i24 v3, s55, v162, v3
	s_lshl_b32 s12, s82, 1
	v_lshl_add_u64 v[2:3], v[2:3], 0, s[12:13]
	v_lshlrev_b32_e32 v148, 4, v173
	v_lshl_add_u64 v[40:41], v[2:3], 0, v[148:149]
	global_load_dwordx4 v[6:9], v[40:41], off
	global_load_dwordx4 v[14:17], v[40:41], off offset:32
	global_load_dwordx4 v[30:33], v[40:41], off offset:64
	global_load_dwordx4 v[34:37], v[40:41], off offset:96
	global_load_dwordx4 v[50:53], v[40:41], off offset:128
	global_load_dwordx4 v[26:29], v[40:41], off offset:160
	global_load_dwordx4 v[22:25], v[40:41], off offset:192
	global_load_dwordx4 v[18:21], v[40:41], off offset:224
	global_load_dwordx4 v[10:13], v[40:41], off offset:256
	global_load_dwordx4 v[42:45], v[40:41], off offset:288
	s_waitcnt lgkmcnt(0)
	global_load_dwordx4 v[2:5], v[40:41], off offset:320
	global_load_dwordx4 v[46:49], v[40:41], off offset:352
	v_and_b32_e32 v40, 32, v172
	v_mov_b32_e32 v39, s55
	s_mul_i32 s86, s0, 0x1800000
	s_mul_hi_i32 s51, s0, 0x1800000
	s_add_u32 s44, s33, s86
	s_addc_u32 s45, s58, s51
	s_lshl_b64 s[56:57], s[0:1], 24
	s_lshl_b32 s79, s46, 7
	s_add_u32 s44, s44, s12
	s_addc_u32 s45, s45, 0
	s_mov_b32 m0, s71
	s_add_u32 s0, s59, s56
	s_addc_u32 s1, s60, s57
	s_lshl_b32 s12, s46, 8
	s_add_u32 s46, s0, s12
	s_addc_u32 s47, s1, 0
	s_lshl_b32 s85, s49, 2
	s_add_i32 s85, s85, 4
	s_or_b32 s48, s56, s48
	s_add_u32 s48, s48, 0x29020000
	s_addc_u32 s49, s57, 0
	s_or_b32 s50, s86, s50
	s_add_u32 s50, s50, 0x23030000
	s_addc_u32 s51, s51, 0
	s_mov_b32 s12, 1
	s_movk_i32 s86, 0xff00
	s_waitcnt vmcnt(0)
	v_lshlrev_b32_e32 v227, 16, v26
	v_lshlrev_b32_e32 v177, 16, v6
	v_and_b32_e32 v174, 0xffff0000, v6
	v_lshlrev_b32_e32 v170, 16, v7
	v_and_b32_e32 v167, 0xffff0000, v7
	v_lshlrev_b32_e32 v180, 16, v8
	v_and_b32_e32 v176, 0xffff0000, v8
	v_lshlrev_b32_e32 v171, 16, v9
	v_and_b32_e32 v169, 0xffff0000, v9
	v_lshlrev_b32_e32 v185, 16, v14
	v_and_b32_e32 v182, 0xffff0000, v14
	v_lshlrev_b32_e32 v179, 16, v15
	v_and_b32_e32 v175, 0xffff0000, v15
	v_lshlrev_b32_e32 v187, 16, v16
	v_and_b32_e32 v183, 0xffff0000, v16
	v_lshlrev_b32_e32 v181, 16, v17
	v_and_b32_e32 v178, 0xffff0000, v17
	v_lshlrev_b32_e32 v201, 16, v34
	v_and_b32_e32 v198, 0xffff0000, v34
	v_lshlrev_b32_e32 v196, 16, v35
	v_and_b32_e32 v192, 0xffff0000, v35
	v_lshlrev_b32_e32 v202, 16, v36
	v_and_b32_e32 v199, 0xffff0000, v36
	v_lshlrev_b32_e32 v197, 16, v37
	v_and_b32_e32 v194, 0xffff0000, v37
	v_and_b32_e32 v228, 0xffff0000, v26
	global_load_dwordx4 v[142:145], v40, s[4:5] offset:704
	global_load_dwordx4 v[130:133], v40, s[4:5] offset:720
	global_load_dwordx4 v[6:9], v40, s[4:5] offset:592
	v_lshlrev_b32_e32 v229, 16, v27
	global_load_dwordx4 v[14:17], v40, s[4:5] offset:576
	v_and_b32_e32 v230, 0xffff0000, v27
	v_lshlrev_b32_e32 v231, 16, v28
	v_and_b32_e32 v232, 0xffff0000, v28
	v_lshlrev_b32_e32 v233, 16, v29
	v_and_b32_e32 v234, 0xffff0000, v29
	global_load_dwordx4 v[34:37], v40, s[4:5] offset:640
	global_load_dwordx4 v[156:159], v40, s[4:5] offset:656
	global_load_dwordx4 v[26:29], v40, s[4:5] offset:528
	v_mul_f32_e32 v209, v174, v174
	v_fmac_f32_e32 v209, v177, v177
	v_fmac_f32_e32 v209, v170, v170
	v_fmac_f32_e32 v209, v167, v167
	v_fmac_f32_e32 v209, v180, v180
	v_fmac_f32_e32 v209, v176, v176
	v_fmac_f32_e32 v209, v171, v171
	v_fmac_f32_e32 v209, v169, v169
	v_fmac_f32_e32 v209, v185, v185
	v_lshlrev_b32_e32 v193, 16, v30
	v_and_b32_e32 v190, 0xffff0000, v30
	v_lshlrev_b32_e32 v188, 16, v31
	v_and_b32_e32 v184, 0xffff0000, v31
	v_lshlrev_b32_e32 v195, 16, v32
	v_and_b32_e32 v191, 0xffff0000, v32
	v_lshlrev_b32_e32 v189, 16, v33
	v_and_b32_e32 v186, 0xffff0000, v33
	v_fmac_f32_e32 v209, v182, v182
	global_load_dwordx4 v[30:33], v40, s[4:5] offset:512
	v_fmac_f32_e32 v209, v179, v179
	v_fmac_f32_e32 v209, v175, v175
	v_fmac_f32_e32 v209, v187, v187
	v_fmac_f32_e32 v209, v183, v183
	v_fmac_f32_e32 v209, v181, v181
	v_fmac_f32_e32 v209, v178, v178
	v_fmac_f32_e32 v209, v193, v193
	v_fmac_f32_e32 v209, v190, v190
	v_fmac_f32_e32 v209, v188, v188
	v_fmac_f32_e32 v209, v184, v184
	v_fmac_f32_e32 v209, v195, v195
	v_fmac_f32_e32 v209, v191, v191
	v_fmac_f32_e32 v209, v189, v189
	v_fmac_f32_e32 v209, v186, v186
	v_fmac_f32_e32 v209, v201, v201
	v_fmac_f32_e32 v209, v198, v198
	v_fmac_f32_e32 v209, v196, v196
	v_fmac_f32_e32 v209, v192, v192
	v_fmac_f32_e32 v209, v202, v202
	v_fmac_f32_e32 v209, v199, v199
	v_fmac_f32_e32 v209, v197, v197
	v_lshlrev_b32_e32 v207, 16, v50
	v_fmac_f32_e32 v209, v194, v194
	v_and_b32_e32 v205, 0xffff0000, v50
	v_fmac_f32_e32 v209, v207, v207
	v_lshlrev_b32_e32 v203, 16, v51
	v_fmac_f32_e32 v209, v205, v205
	v_and_b32_e32 v200, 0xffff0000, v51
	v_fmac_f32_e32 v209, v203, v203
	v_lshlrev_b32_e32 v208, 16, v52
	v_fmac_f32_e32 v209, v200, v200
	v_and_b32_e32 v206, 0xffff0000, v52
	v_fmac_f32_e32 v209, v208, v208
	v_lshlrev_b32_e32 v204, 16, v53
	v_fmac_f32_e32 v209, v206, v206
	v_and_b32_e32 v226, 0xffff0000, v53
	v_fmac_f32_e32 v209, v204, v204
	v_fmac_f32_e32 v209, v226, v226
	v_fmac_f32_e32 v209, v227, v227
	v_fmac_f32_e32 v209, v228, v228
	v_fmac_f32_e32 v209, v229, v229
	v_fmac_f32_e32 v209, v230, v230
	global_load_dwordx4 v[110:113], v40, s[4:5] offset:16
	global_load_dwordx4 v[114:117], v40, s[4:5]
	global_load_dwordx4 v[102:105], v40, s[4:5] offset:80
	global_load_dwordx4 v[106:109], v40, s[4:5] offset:64
	global_load_dwordx4 v[94:97], v40, s[4:5] offset:144
	global_load_dwordx4 v[98:101], v40, s[4:5] offset:128
	global_load_dwordx4 v[86:89], v40, s[4:5] offset:208
	global_load_dwordx4 v[90:93], v40, s[4:5] offset:192
	global_load_dwordx4 v[78:81], v40, s[4:5] offset:272
	global_load_dwordx4 v[82:85], v40, s[4:5] offset:256
	global_load_dwordx4 v[70:73], v40, s[4:5] offset:336
	global_load_dwordx4 v[74:77], v40, s[4:5] offset:320
	global_load_dwordx4 v[62:65], v40, s[4:5] offset:400
	global_load_dwordx4 v[66:69], v40, s[4:5] offset:384
	global_load_dwordx4 v[54:57], v40, s[4:5] offset:464
	global_load_dwordx4 v[58:61], v40, s[4:5] offset:448
	v_fmac_f32_e32 v209, v231, v231
	v_fmac_f32_e32 v209, v232, v232
	v_fmac_f32_e32 v209, v233, v233
	v_fmac_f32_e32 v209, v234, v234
	s_waitcnt vmcnt(29)
	v_lshlrev_b32_e32 v235, 16, v22
	v_and_b32_e32 v236, 0xffff0000, v22
	v_fmac_f32_e32 v209, v235, v235
	v_lshlrev_b32_e32 v237, 16, v23
	v_fmac_f32_e32 v209, v236, v236
	v_and_b32_e32 v238, 0xffff0000, v23
	v_fmac_f32_e32 v209, v237, v237
	v_lshlrev_b32_e32 v239, 16, v24
	v_fmac_f32_e32 v209, v238, v238
	v_and_b32_e32 v240, 0xffff0000, v24
	v_fmac_f32_e32 v209, v239, v239
	v_lshlrev_b32_e32 v241, 16, v25
	v_fmac_f32_e32 v209, v240, v240
	v_and_b32_e32 v242, 0xffff0000, v25
	v_fmac_f32_e32 v209, v241, v241
	v_fmac_f32_e32 v209, v242, v242
	s_waitcnt vmcnt(28)
	v_lshlrev_b32_e32 v243, 16, v18
	v_and_b32_e32 v244, 0xffff0000, v18
	v_fmac_f32_e32 v209, v243, v243
	v_lshlrev_b32_e32 v245, 16, v19
	v_fmac_f32_e32 v209, v244, v244
	v_and_b32_e32 v246, 0xffff0000, v19
	v_fmac_f32_e32 v209, v245, v245
	v_lshlrev_b32_e32 v247, 16, v20
	v_fmac_f32_e32 v209, v246, v246
	v_and_b32_e32 v248, 0xffff0000, v20
	v_fmac_f32_e32 v209, v247, v247
	v_lshlrev_b32_e32 v249, 16, v21
	v_fmac_f32_e32 v209, v248, v248
	v_and_b32_e32 v250, 0xffff0000, v21
	v_fmac_f32_e32 v209, v249, v249
	s_waitcnt vmcnt(27)
	v_lshlrev_b32_e32 v223, 16, v10
	s_waitcnt vmcnt(25)
	v_lshlrev_b32_e32 v222, 16, v2
	v_fmac_f32_e32 v209, v250, v250
	s_waitcnt vmcnt(18)
	v_mov_b32_e32 v150, v158
	v_mov_b32_e32 v158, v156
	v_lshlrev_b32_e32 v156, 16, v3
	v_and_b32_e32 v160, 0xffff0000, v3
	v_and_b32_e32 v225, 0xffff0000, v10
	v_and_b32_e32 v224, 0xffff0000, v2
	v_pk_mul_f32 v[2:3], v[222:223], v[222:223]
	v_mov_b32_e32 v134, v144
	v_mov_b32_e32 v140, v142
	v_lshlrev_b32_e32 v142, 16, v5
	s_waitcnt vmcnt(17)
	v_mov_b32_e32 v151, v28
	v_and_b32_e32 v144, 0xffff0000, v5
	v_mov_b32_e32 v28, v159
	v_lshlrev_b32_e32 v152, 16, v4
	v_mov_b32_e32 v159, v26
	v_and_b32_e32 v154, 0xffff0000, v4
	v_mov_b32_e32 v26, v157
	v_lshlrev_b32_e32 v157, 16, v11
	v_add_f32_e32 v3, v3, v209
	v_pk_mul_f32 v[4:5], v[224:225], v[224:225]
	v_lshlrev_b32_e32 v119, 16, v45
	v_and_b32_e32 v121, 0xffff0000, v45
	v_lshlrev_b32_e32 v125, 16, v44
	v_and_b32_e32 v127, 0xffff0000, v44
	v_pk_mul_f32 v[44:45], v[156:157], v[156:157]
	v_and_b32_e32 v161, 0xffff0000, v11
	v_add_f32_e32 v3, v5, v3
	v_mov_b32_e32 v122, v132
	v_mov_b32_e32 v128, v130
	v_lshlrev_b32_e32 v130, 16, v47
	v_and_b32_e32 v132, 0xffff0000, v47
	v_lshlrev_b32_e32 v136, 16, v46
	v_and_b32_e32 v138, 0xffff0000, v46
	v_lshlrev_b32_e32 v153, 16, v12
	v_pk_mul_f32 v[46:47], v[160:161], v[160:161]
	v_add_f32_e32 v3, v45, v3
	v_mov_b32_e32 v123, v8
	v_mov_b32_e32 v8, v133
	v_mov_b32_e32 v129, v6
	v_mov_b32_e32 v6, v131
	v_lshlrev_b32_e32 v131, 16, v43
	v_and_b32_e32 v133, 0xffff0000, v43
	v_lshlrev_b32_e32 v137, 16, v42
	v_and_b32_e32 v139, 0xffff0000, v42
	v_pk_mul_f32 v[42:43], v[152:153], v[152:153]
	v_and_b32_e32 v155, 0xffff0000, v12
	v_add_f32_e32 v3, v47, v3
	v_mov_b32_e32 v141, v14
	v_mov_b32_e32 v14, v143
	v_lshlrev_b32_e32 v143, 16, v13
	v_pk_mul_f32 v[220:221], v[154:155], v[154:155]
	v_add_f32_e32 v3, v43, v3
	v_mov_b32_e32 v135, v16
	v_mov_b32_e32 v16, v145
	v_pk_mul_f32 v[216:217], v[142:143], v[142:143]
	v_and_b32_e32 v145, 0xffff0000, v13
	v_add_f32_e32 v3, v221, v3
	v_pk_mul_f32 v[218:219], v[144:145], v[144:145]
	v_add_f32_e32 v3, v217, v3
	v_pk_mul_f32 v[212:213], v[136:137], v[136:137]
	v_add_f32_e32 v3, v219, v3
	v_pk_mul_f32 v[214:215], v[138:139], v[138:139]
	v_add_f32_e32 v3, v213, v3
	v_add_f32_e32 v3, v215, v3
	v_fmac_f32_e32 v3, v131, v131
	v_fmac_f32_e32 v3, v133, v133
	v_fmac_f32_e32 v3, v125, v125
	v_fmac_f32_e32 v3, v127, v127
	v_fmac_f32_e32 v3, v119, v119
	v_fmac_f32_e32 v3, v121, v121
	v_add_f32_e32 v2, v2, v3
	v_add_f32_e32 v43, v4, v2
	v_add_f32_e32 v43, v44, v43
	v_add_f32_e32 v43, v46, v43
	v_add_f32_e32 v209, v42, v43
	v_add_f32_e32 v209, v220, v209
	v_add_f32_e32 v209, v216, v209
	v_add_f32_e32 v209, v218, v209
	v_mov_b32_e32 v218, v132
	v_mov_b32_e32 v219, v130
	v_add_f32_e32 v209, v212, v209
	v_lshlrev_b64 v[18:19], 8, v[38:39]
	v_lshlrev_b32_e32 v124, 16, v48
	v_and_b32_e32 v126, 0xffff0000, v48
	v_pk_mul_f32 v[218:219], v[218:219], v[218:219]
	s_waitcnt vmcnt(16)
	v_mov_b32_e32 v213, v32
	v_add_f32_e32 v32, v214, v209
	v_lshl_add_u64 v[18:19], s[10:11], 0, v[18:19]
	v_lshlrev_b32_e32 v20, 6, v173
	v_mov_b32_e32 v21, v149
	v_mov_b32_e32 v216, v126
	v_mov_b32_e32 v217, v124
	v_add_f32_e32 v32, v219, v32
	v_lshl_add_u64 v[210:211], v[18:19], 0, v[20:21]
	v_lshlrev_b32_e32 v118, 16, v49
	v_and_b32_e32 v120, 0xffff0000, v49
	v_pk_mul_f32 v[216:217], v[216:217], v[216:217]
	v_add_f32_e32 v32, v218, v32
	global_load_dwordx4 v[18:21], v[210:211], off offset:48
	global_load_dwordx4 v[22:25], v[210:211], off offset:32
	global_load_dwordx4 v[38:41], v[210:211], off offset:16
	global_load_dwordx4 v[50:53], v[210:211], off
	global_load_dwordx4 v[2:5], v[210:211], off offset:176
	global_load_dwordx4 v[10:13], v[210:211], off offset:160
	global_load_dwordx4 v[42:45], v[210:211], off offset:144
	global_load_dwordx4 v[46:49], v[210:211], off offset:128
	v_mov_b32_e32 v210, v120
	v_mov_b32_e32 v211, v118
	v_add_f32_e32 v32, v217, v32
	v_pk_mul_f32 v[210:211], v[210:211], v[210:211]
	v_add_f32_e32 v32, v216, v32
	v_add_f32_e32 v32, v211, v32
	v_add_f32_e32 v32, v210, v32
	v_mov_b32_e32 v212, v36
	v_mov_b32_e32 v36, v32
	s_nop 1
	v_permlane32_swap_b32_e32 v32, v36
	v_add_f32_e32 v32, v32, v36
	v_fmamk_f32 v32, v32, 0x3baaaaab, v163
	v_mul_f32_e32 v36, 0x4b800000, v32
	v_cmp_gt_f32_e32 vcc, s69, v32
	s_nop 1
	v_cndmask_b32_e32 v32, v32, v36, vcc
	v_rsq_f32_e32 v209, v32
	v_mov_b32_e32 v32, v37
	v_mov_b32_e32 v37, v30
	v_mov_b32_e32 v36, v34
	v_mul_f32_e32 v30, 0x45800000, v209
	v_cndmask_b32_e32 v30, v209, v30, vcc
	v_mul_f32_e32 v34, 0x3dd53b94, v30
	s_waitcnt vmcnt(22)
	v_mul_f32_e32 v30, v114, v34
	v_mul_f32_e32 v114, v30, v177
	v_mul_f32_e32 v30, v110, v34
	v_mul_f32_e32 v110, v30, v180
	v_mul_f32_e32 v30, v115, v34
	v_mul_f32_e32 v115, v30, v174
	v_mul_f32_e32 v30, v111, v34
	v_mul_f32_e32 v111, v30, v176
	v_mul_f32_e32 v30, v116, v34
	v_mul_f32_e32 v116, v30, v170
	v_mul_f32_e32 v30, v112, v34
	v_mul_f32_e32 v112, v30, v171
	v_mul_f32_e32 v30, v117, v34
	v_mul_f32_e32 v117, v30, v167
	v_mul_f32_e32 v30, v113, v34
	v_mul_f32_e32 v113, v30, v169
	s_waitcnt vmcnt(20)
	v_mul_f32_e32 v30, v106, v34
	v_mul_f32_e32 v106, v30, v185
	v_mul_f32_e32 v30, v102, v34
	v_mul_f32_e32 v167, v30, v187
	v_mul_f32_e32 v30, v107, v34
	v_mul_f32_e32 v102, v30, v182
	v_mul_f32_e32 v30, v103, v34
	v_mul_f32_e32 v107, v30, v183
	v_mul_f32_e32 v30, v108, v34
	v_mul_f32_e32 v103, v30, v179
	v_mul_f32_e32 v30, v104, v34
	v_mul_f32_e32 v108, v30, v181
	v_mul_f32_e32 v30, v109, v34
	v_mul_f32_e32 v104, v30, v175
	v_mul_f32_e32 v30, v105, v34
	v_mul_f32_e32 v105, v30, v178
	s_waitcnt vmcnt(18)
	v_mul_f32_e32 v30, v98, v34
	v_mul_f32_e32 v109, v30, v193
	v_mul_f32_e32 v30, v94, v34
	v_mul_f32_e32 v94, v30, v195
	v_mul_f32_e32 v30, v99, v34
	v_mul_f32_e32 v169, v30, v190
	v_mul_f32_e32 v30, v95, v34
	v_mul_f32_e32 v95, v30, v191
	v_mul_f32_e32 v30, v100, v34
	v_mul_f32_e32 v170, v30, v188
	v_mul_f32_e32 v30, v96, v34
	v_mul_f32_e32 v96, v30, v189
	v_mul_f32_e32 v30, v101, v34
	v_mul_f32_e32 v171, v30, v184
	v_mul_f32_e32 v30, v97, v34
	v_mul_f32_e32 v97, v30, v186
	s_waitcnt vmcnt(16)
	v_mul_f32_e32 v30, v90, v34
	v_mul_f32_e32 v90, v30, v201
	v_mul_f32_e32 v30, v86, v34
	v_mul_f32_e32 v86, v30, v202
	v_mul_f32_e32 v30, v91, v34
	v_mul_f32_e32 v91, v30, v198
	v_mul_f32_e32 v30, v87, v34
	v_mul_f32_e32 v87, v30, v199
	v_mul_f32_e32 v30, v92, v34
	v_mul_f32_e32 v92, v30, v196
	v_mul_f32_e32 v30, v88, v34
	v_mul_f32_e32 v88, v30, v197
	v_mul_f32_e32 v30, v93, v34
	v_mul_f32_e32 v93, v30, v192
	v_mul_f32_e32 v30, v89, v34
	v_mul_f32_e32 v89, v30, v194
	s_waitcnt vmcnt(14)
	v_mul_f32_e32 v30, v82, v34
	v_mul_f32_e32 v82, v30, v207
	v_mul_f32_e32 v30, v34, v78
	v_mul_f32_e32 v78, v30, v208
	v_mul_f32_e32 v30, v83, v34
	v_mul_f32_e32 v83, v30, v205
	v_mul_f32_e32 v30, v34, v79
	v_mul_f32_e32 v79, v30, v206
	v_mul_f32_e32 v30, v84, v34
	v_mul_f32_e32 v84, v30, v203
	v_mul_f32_e32 v30, v34, v80
	v_mul_f32_e32 v80, v30, v204
	v_mul_f32_e32 v30, v85, v34
	v_mul_f32_e32 v85, v30, v200
	v_mul_f32_e32 v30, v34, v81
	v_mul_f32_e32 v81, v30, v226
	s_waitcnt vmcnt(12)
	v_mul_f32_e32 v30, v34, v74
	v_mul_f32_e32 v74, v30, v227
	v_mul_f32_e32 v30, v34, v70
	v_mul_f32_e32 v70, v30, v231
	v_mul_f32_e32 v30, v34, v75
	v_mul_f32_e32 v75, v30, v228
	v_mul_f32_e32 v30, v34, v71
	v_mul_f32_e32 v71, v30, v232
	v_mul_f32_e32 v30, v34, v76
	v_mul_f32_e32 v76, v30, v229
	v_mul_f32_e32 v30, v34, v72
	v_mul_f32_e32 v72, v30, v233
	v_mul_f32_e32 v30, v34, v77
	v_mul_f32_e32 v77, v30, v230
	v_mul_f32_e32 v30, v34, v73
	v_mul_f32_e32 v73, v30, v234
	s_waitcnt vmcnt(10)
	v_mul_f32_e32 v30, v34, v66
	v_mul_f32_e32 v174, v30, v235
	v_mul_f32_e32 v30, v34, v62
	v_mul_f32_e32 v175, v30, v239
	v_mul_f32_e32 v30, v34, v67
	v_mul_f32_e32 v176, v30, v236
	v_mul_f32_e32 v30, v34, v63
	v_mul_f32_e32 v177, v30, v240
	v_mul_f32_e32 v30, v34, v68
	v_mul_f32_e32 v68, v30, v237
	v_mul_f32_e32 v30, v34, v64
	v_mul_f32_e32 v178, v30, v241
	v_mul_f32_e32 v30, v34, v69
	v_mul_f32_e32 v69, v30, v238
	v_mul_f32_e32 v30, v34, v65
	v_mul_f32_e32 v179, v30, v242
	s_waitcnt vmcnt(8)
	v_mul_f32_e32 v30, v34, v58
	v_mul_f32_e32 v180, v30, v243
	v_mul_f32_e32 v30, v34, v54
	v_mul_f32_e32 v181, v30, v247
	v_mul_f32_e32 v30, v34, v59
	v_mul_f32_e32 v182, v30, v244
	v_mul_f32_e32 v30, v34, v55
	v_mul_f32_e32 v183, v30, v248
	v_mul_f32_e32 v30, v34, v60
	v_mul_f32_e32 v184, v30, v245
	v_mul_f32_e32 v30, v34, v56
	v_mul_f32_e32 v185, v30, v249
	v_mul_f32_e32 v30, v34, v61
	v_mul_f32_e32 v186, v30, v246
	v_mul_f32_e32 v30, v34, v57
	v_pk_mul_f32 v[36:37], v[34:35], v[36:37] op_sel_hi:[0,1]
	v_mul_f32_e32 v187, v30, v250
	v_pk_mul_f32 v[36:37], v[36:37], v[222:223]
	v_mov_b32_e32 v30, v35
	v_pk_mul_f32 v[54:55], v[34:35], v[158:159] op_sel_hi:[0,1]
	v_pk_mul_f32 v[30:31], v[34:35], v[30:31] op_sel_hi:[0,1]
	v_pk_mul_f32 v[26:27], v[34:35], v[26:27] op_sel_hi:[0,1]
	v_pk_mul_f32 v[56:57], v[34:35], v[212:213] op_sel_hi:[0,1]
	v_pk_mul_f32 v[58:59], v[34:35], v[150:151] op_sel_hi:[0,1]
	v_pk_mul_f32 v[32:33], v[34:35], v[32:33] op_sel_hi:[0,1]
	v_pk_mul_f32 v[28:29], v[34:35], v[28:29] op_sel_hi:[0,1]
	v_pk_mul_f32 v[60:61], v[34:35], v[140:141] op_sel_hi:[0,1]
	v_pk_mul_f32 v[62:63], v[34:35], v[128:129] op_sel_hi:[0,1]
	v_pk_mul_f32 v[14:15], v[34:35], v[14:15] op_sel_hi:[0,1]
	v_pk_mul_f32 v[6:7], v[34:35], v[6:7] op_sel_hi:[0,1]
	v_pk_mul_f32 v[64:65], v[34:35], v[134:135] op_sel_hi:[0,1]
	v_pk_mul_f32 v[66:67], v[34:35], v[122:123] op_sel_hi:[0,1]
	v_pk_mul_f32 v[16:17], v[34:35], v[16:17] op_sel_hi:[0,1]
	v_pk_mul_f32 v[8:9], v[34:35], v[8:9] op_sel_hi:[0,1]
	s_waitcnt vmcnt(4)
	v_pk_mul_f32 v[34:35], v[36:37], v[50:51] op_sel:[1,0] op_sel_hi:[0,1]
	v_pk_mul_f32 v[30:31], v[30:31], v[224:225]
	v_pk_mul_f32 v[64:65], v[64:65], v[130:131]
	v_sub_f32_e32 v130, v34, v35
	v_pk_mul_f32 v[34:35], v[36:37], v[50:51]
	v_pk_mul_f32 v[56:57], v[56:57], v[156:157]
	v_add_f32_e32 v36, v35, v34
	v_pk_mul_f32 v[34:35], v[30:31], v[52:53] op_sel:[1,0] op_sel_hi:[0,1]
	v_pk_mul_f32 v[30:31], v[30:31], v[52:53]
	v_sub_f32_e32 v34, v34, v35
	v_add_f32_e32 v35, v31, v30
	v_pk_mul_f32 v[30:31], v[56:57], v[38:39] op_sel:[1,0] op_sel_hi:[0,1]
	v_pk_mul_f32 v[32:33], v[32:33], v[160:161]
	v_sub_f32_e32 v37, v30, v31
	v_pk_mul_f32 v[30:31], v[56:57], v[38:39]
	v_pk_mul_f32 v[54:55], v[54:55], v[152:153]
	v_add_f32_e32 v38, v31, v30
	v_pk_mul_f32 v[30:31], v[32:33], v[40:41] op_sel:[1,0] op_sel_hi:[0,1]
	v_sub_f32_e32 v39, v30, v31
	v_pk_mul_f32 v[30:31], v[32:33], v[40:41]
	v_pk_mul_f32 v[26:27], v[26:27], v[154:155]
	v_add_f32_e32 v32, v31, v30
	v_pk_mul_f32 v[30:31], v[54:55], v[22:23] op_sel:[1,0] op_sel_hi:[0,1]
	v_pk_mul_f32 v[22:23], v[54:55], v[22:23]
	v_sub_f32_e32 v30, v30, v31
	v_add_f32_e32 v31, v23, v22
	v_pk_mul_f32 v[22:23], v[26:27], v[24:25] op_sel:[1,0] op_sel_hi:[0,1]
	v_pk_mul_f32 v[58:59], v[58:59], v[142:143]
	v_sub_f32_e32 v33, v22, v23
	v_pk_mul_f32 v[22:23], v[26:27], v[24:25]
	v_pk_mul_f32 v[28:29], v[28:29], v[144:145]
	v_add_f32_e32 v24, v23, v22
	v_pk_mul_f32 v[22:23], v[58:59], v[18:19] op_sel:[1,0] op_sel_hi:[0,1]
	v_pk_mul_f32 v[18:19], v[58:59], v[18:19]
	v_sub_f32_e32 v22, v22, v23
	v_add_f32_e32 v23, v19, v18
	v_pk_mul_f32 v[18:19], v[28:29], v[20:21] op_sel:[1,0] op_sel_hi:[0,1]
	v_pk_mul_f32 v[60:61], v[60:61], v[136:137]
	v_sub_f32_e32 v25, v18, v19
	v_pk_mul_f32 v[18:19], v[28:29], v[20:21]
	v_pk_mul_f32 v[14:15], v[14:15], v[138:139]
	v_add_f32_e32 v20, v19, v18
	s_waitcnt vmcnt(0)
	v_pk_mul_f32 v[18:19], v[60:61], v[46:47] op_sel:[1,0] op_sel_hi:[0,1]
	v_sub_f32_e32 v21, v18, v19
	v_pk_mul_f32 v[18:19], v[60:61], v[46:47]
	v_pk_mul_f32 v[16:17], v[16:17], v[132:133]
	v_add_f32_e32 v26, v19, v18
	v_pk_mul_f32 v[18:19], v[14:15], v[48:49] op_sel:[1,0] op_sel_hi:[0,1]
	v_pk_mul_f32 v[14:15], v[14:15], v[48:49]
	v_sub_f32_e32 v18, v18, v19
	v_add_f32_e32 v19, v15, v14
	v_pk_mul_f32 v[14:15], v[64:65], v[42:43] op_sel:[1,0] op_sel_hi:[0,1]
	v_sub_f32_e32 v27, v14, v15
	v_pk_mul_f32 v[14:15], v[64:65], v[42:43]
	v_pk_mul_f32 v[62:63], v[62:63], v[124:125]
	v_add_f32_e32 v28, v15, v14
	v_pk_mul_f32 v[14:15], v[16:17], v[44:45] op_sel:[1,0] op_sel_hi:[0,1]
	v_sub_f32_e32 v29, v14, v15
	v_pk_mul_f32 v[14:15], v[16:17], v[44:45]
	v_pk_mul_f32 v[6:7], v[6:7], v[126:127]
	v_add_f32_e32 v16, v15, v14
	v_pk_mul_f32 v[14:15], v[62:63], v[10:11] op_sel:[1,0] op_sel_hi:[0,1]
	v_pk_mul_f32 v[10:11], v[62:63], v[10:11]
	v_pk_mul_f32 v[66:67], v[66:67], v[118:119]
	v_sub_f32_e32 v14, v14, v15
	v_add_f32_e32 v15, v11, v10
	v_pk_mul_f32 v[10:11], v[6:7], v[12:13] op_sel:[1,0] op_sel_hi:[0,1]
	v_pk_mul_f32 v[6:7], v[6:7], v[12:13]
	v_pk_mul_f32 v[8:9], v[8:9], v[120:121]
	v_sub_f32_e32 v10, v10, v11
	v_add_f32_e32 v11, v7, v6
	v_pk_mul_f32 v[6:7], v[66:67], v[2:3] op_sel:[1,0] op_sel_hi:[0,1]
	v_pk_mul_f32 v[2:3], v[66:67], v[2:3]
	v_sub_f32_e32 v6, v6, v7
	v_add_f32_e32 v7, v3, v2
	v_pk_mul_f32 v[2:3], v[8:9], v[4:5] op_sel:[1,0] op_sel_hi:[0,1]
	v_sub_f32_e32 v12, v2, v3
	v_pk_mul_f32 v[2:3], v[8:9], v[4:5]
	v_cvt_pk_bf16_f32 v98, v114, v115
	v_cvt_pk_bf16_f32 v99, v116, v117
	v_cvt_pk_bf16_f32 v100, v110, v111
	v_cvt_pk_bf16_f32 v101, v112, v113
	v_cvt_pk_bf16_f32 v102, v106, v102
	s_nop 0
	v_add_f32_e32 v2, v3, v2
	v_cvt_pk_bf16_f32 v103, v103, v104
	v_cvt_pk_bf16_f32 v104, v167, v107
	v_cvt_pk_bf16_f32 v105, v108, v105
	v_cvt_pk_bf16_f32 v106, v109, v169
	v_cvt_pk_bf16_f32 v107, v170, v171
	v_cvt_pk_bf16_f32 v108, v94, v95
	v_cvt_pk_bf16_f32 v109, v96, v97
	v_cvt_pk_bf16_f32 v110, v90, v91
	v_cvt_pk_bf16_f32 v111, v92, v93
	v_cvt_pk_bf16_f32 v112, v86, v87
	v_cvt_pk_bf16_f32 v113, v88, v89
	v_cvt_pk_bf16_f32 v114, v82, v83
	v_cvt_pk_bf16_f32 v115, v84, v85
	v_cvt_pk_bf16_f32 v116, v78, v79
	v_cvt_pk_bf16_f32 v117, v80, v81
	v_cvt_pk_bf16_f32 v118, v74, v75
	v_cvt_pk_bf16_f32 v119, v76, v77
	v_cvt_pk_bf16_f32 v120, v70, v71
	v_cvt_pk_bf16_f32 v121, v72, v73
	v_cvt_pk_bf16_f32 v122, v174, v176
	v_cvt_pk_bf16_f32 v123, v68, v69
	v_cvt_pk_bf16_f32 v124, v175, v177
	v_cvt_pk_bf16_f32 v125, v178, v179
	v_cvt_pk_bf16_f32 v126, v180, v182
	v_cvt_pk_bf16_f32 v127, v184, v186
	v_cvt_pk_bf16_f32 v128, v181, v183
	v_cvt_pk_bf16_f32 v129, v185, v187
	v_cvt_pk_bf16_f32 v130, v130, v34
	v_cvt_pk_bf16_f32 v131, v37, v39
	v_cvt_pk_bf16_f32 v132, v30, v33
	v_cvt_pk_bf16_f32 v133, v22, v25
	v_cvt_pk_bf16_f32 v134, v21, v18
	v_cvt_pk_bf16_f32 v135, v27, v29
	v_cvt_pk_bf16_f32 v136, v14, v10
	v_cvt_pk_bf16_f32 v137, v6, v12
	v_cvt_pk_bf16_f32 v138, v36, v35
	v_cvt_pk_bf16_f32 v139, v38, v32
	v_cvt_pk_bf16_f32 v140, v31, v24
	v_cvt_pk_bf16_f32 v141, v23, v20
	v_cvt_pk_bf16_f32 v142, v26, v19
	v_cvt_pk_bf16_f32 v143, v28, v16
	v_cvt_pk_bf16_f32 v144, v15, v11
	v_cvt_pk_bf16_f32 v145, v7, v2
	v_mul_hi_i32 v2, v172, s70
	v_lshrrev_b32_e32 v3, 31, v2
	v_ashrrev_i32_e32 v2, 2, v2
	v_add_u32_e32 v2, v2, v3
	v_mul_lo_u32 v3, v2, 24
	v_sub_u32_e32 v3, v172, v3
	v_bitop3_b32 v3, v2, v3, 7 bitop3:0x6c
	v_mul_lo_u32 v2, v2, s68
	v_lshl_add_u32 v2, v3, 4, v2
	v_add_u32_e32 v3, 0x200, v172
	v_mul_hi_i32 v4, v3, s70
	v_lshrrev_b32_e32 v5, 31, v4
	v_ashrrev_i32_e32 v4, 2, v4
	v_add_u32_e32 v4, v4, v5
	v_mul_lo_u32 v5, v4, 24
	v_sub_u32_e32 v5, v3, v5
	v_bitop3_b32 v5, v4, v5, 7 bitop3:0x6c
	v_mul_lo_u32 v4, v4, s68
	v_lshl_add_u32 v4, v5, 4, v4
	v_add_u32_e32 v5, 0x400, v172
	v_mul_hi_i32 v6, v5, s70
	v_lshrrev_b32_e32 v7, 31, v6
	v_ashrrev_i32_e32 v6, 2, v6
	v_add_u32_e32 v6, v6, v7
	v_mul_lo_u32 v7, v6, 24
	v_sub_u32_e32 v5, v5, v7
	v_bitop3_b32 v5, v6, v5, 7 bitop3:0x6c
	v_mul_lo_u32 v6, v6, s68
	v_ashrrev_i32_e32 v9, 4, v172
	v_lshl_add_u32 v6, v5, 4, v6
	v_bfe_u32 v5, v172, 2, 2
	v_lshrrev_b32_e32 v7, 1, v172
	v_and_b32_e32 v10, 0x1ffff0, v9
	v_lshrrev_b32_e32 v9, 1, v9
	v_ashrrev_i32_e32 v3, 4, v3
	v_and_or_b32 v5, v7, 8, v5
	v_and_b32_e32 v7, 0x60, v172
	v_lshlrev_b32_e32 v8, 3, v172
	v_and_b32_e32 v9, 4, v9
	v_and_b32_e32 v11, 0x1ffff0, v3
	v_lshrrev_b32_e32 v3, 1, v3
	v_and_or_b32 v7, v8, 24, v7
	v_or3_b32 v9, v10, v9, v5
	v_and_b32_e32 v3, 4, v3
	s_barrier
	global_load_lds_dwordx4 v2, s[44:45]
	s_mov_b32 m0, s72
	v_lshlrev_b32_e32 v7, 1, v7
	v_lshlrev_b32_e32 v10, 11, v9
	v_or3_b32 v3, v11, v3, v5
	global_load_lds_dwordx4 v4, s[44:45]
	s_mov_b32 m0, s73
	v_or_b32_e32 v9, v10, v7
	v_lshlrev_b32_e32 v11, 11, v3
	global_load_lds_dwordx4 v6, s[44:45]
	s_mov_b32 m0, s64
	v_or_b32_e32 v3, v11, v7
	global_load_lds_dwordx4 v9, s[46:47]
	s_mov_b32 m0, s74
	v_lshlrev_b32_e32 v13, 1, v172
	global_load_lds_dwordx4 v3, s[46:47]
	v_lshlrev_b32_e32 v9, 4, v172
	v_and_b32_e32 v14, 32, v13
	v_or_b32_e32 v3, 32, v148
	v_mul_u32_u24_e32 v5, 0x180, v168
	v_and_b32_e32 v7, 0x70, v9
	v_and_b32_e32 v12, 0xc0, v9
	v_and_or_b32 v8, v8, s75, v14
	v_and_b32_e32 v167, 63, v172
	v_bitop3_b32 v169, v3, v5, v7 bitop3:0xde
	v_or_b32_e32 v3, 64, v148
	v_add3_u32 v172, v12, 0, v8
	v_and_b32_e32 v12, 0xc0, v13
	v_and_b32_e32 v13, 48, v9
	v_bitop3_b32 v170, v3, v5, v7 bitop3:0xde
	v_or_b32_e32 v3, 0x60, v148
	v_or3_b32 v8, v11, v12, v13
	v_mov_b32_e32 v9, v149
	v_bitop3_b32 v161, v148, v5, v7 bitop3:0xde
	v_bitop3_b32 v171, v3, v5, v7 bitop3:0xde
	v_mov_b32_e32 v3, v149
	v_mov_b32_e32 v5, v149
	v_mov_b32_e32 v7, v149
	v_mul_i32_i24_e32 v15, -4, v173
	v_lshl_add_u64 v[150:151], s[48:49], 0, v[8:9]
	v_or3_b32 v8, v10, v12, v13
	v_mov_b32_e32 v16, v149
	v_mov_b32_e32 v17, v149
	v_lshl_add_u32 v160, v168, 2, s65
	v_lshl_add_u64 v[152:153], s[48:49], 0, v[8:9]
	v_lshl_add_u64 v[154:155], s[50:51], 0, v[6:7]
	v_lshl_add_u64 v[156:157], s[50:51], 0, v[4:5]
	v_lshl_add_u64 v[158:159], s[50:51], 0, v[2:3]
	v_add3_u32 v168, s63, v15, v168
	v_mov_b32_e32 v2, v149
	v_mov_b32_e32 v4, v149
	v_mov_b32_e32 v6, v149
	v_mov_b32_e32 v8, v149
	v_mov_b32_e32 v10, v149
	v_mov_b32_e32 v11, v149
	v_mov_b32_e32 v12, v149
	v_mov_b32_e32 v13, v149
	v_mov_b32_e32 v14, v149
	v_mov_b32_e32 v15, v149
	v_mov_b64_e32 v[32:33], v[16:17]
	v_mov_b64_e32 v[48:49], v[16:17]
	v_mov_b64_e32 v[64:65], v[16:17]
	v_cmp_gt_u32_e64 s[0:1], 32, v167
	v_mov_b32_e32 v173, 0xf149f2ca
	v_mov_b64_e32 v[30:31], v[14:15]
	v_mov_b64_e32 v[28:29], v[12:13]
	v_mov_b64_e32 v[26:27], v[10:11]
	v_mov_b64_e32 v[24:25], v[8:9]
	v_mov_b64_e32 v[22:23], v[6:7]
	v_mov_b64_e32 v[20:21], v[4:5]
	v_mov_b64_e32 v[18:19], v[2:3]
	v_mov_b64_e32 v[46:47], v[14:15]
	v_mov_b64_e32 v[44:45], v[12:13]
	v_mov_b64_e32 v[42:43], v[10:11]
	v_mov_b64_e32 v[40:41], v[8:9]
	v_mov_b64_e32 v[38:39], v[6:7]
	v_mov_b64_e32 v[36:37], v[4:5]
	v_mov_b64_e32 v[34:35], v[2:3]
	v_mov_b64_e32 v[62:63], v[14:15]
	v_mov_b64_e32 v[60:61], v[12:13]
	v_mov_b64_e32 v[58:59], v[10:11]
	v_mov_b64_e32 v[56:57], v[8:9]
	v_mov_b64_e32 v[54:55], v[6:7]
	v_mov_b64_e32 v[52:53], v[4:5]
	v_mov_b64_e32 v[50:51], v[2:3]
	v_mov_b32_e32 v174, 0

.LBB0_945:
	s_or_b64 exec, exec, s[0:1]
	s_lshl_b32 s55, s80, 8
	s_and_b32 s0, s81, 15
	s_add_i32 s55, s55, s63
	s_lshl_b32 s54, s0, 8
	v_mov_b32_e32 v168, v1
	s_ashr_i32 s0, s55, 31
	s_add_u32 s52, s52, s55
	v_and_b32_e32 v167, 31, v168
	v_or_b32_e32 v30, s52, v167
	v_mov_b64_e32 v[2:3], s[6:7]
	s_addc_u32 s53, s53, s0
	v_mad_u64_u32 v[2:3], s[0:1], v30, s68, v[2:3]
	v_bfe_u32 v169, v168, 5, 1
	v_mad_i32_i24 v3, s53, v162, v3
	s_lshl_b32 s12, s82, 1
	v_lshl_add_u64 v[2:3], v[2:3], 0, s[12:13]
	v_lshlrev_b32_e32 v148, 4, v169
	v_lshl_add_u64 v[44:45], v[2:3], 0, v[148:149]
	global_load_dwordx4 v[32:35], v[44:45], off
	global_load_dwordx4 v[36:39], v[44:45], off offset:32
	global_load_dwordx4 v[26:29], v[44:45], off offset:64
	global_load_dwordx4 v[22:25], v[44:45], off offset:96
	global_load_dwordx4 v[18:21], v[44:45], off offset:128
	global_load_dwordx4 v[14:17], v[44:45], off offset:160
	global_load_dwordx4 v[10:13], v[44:45], off offset:192
	v_and_b32_e32 v118, 32, v168
	global_load_dwordx4 v[6:9], v118, s[4:5] offset:576
	s_waitcnt lgkmcnt(0)
	global_load_dwordx4 v[2:5], v118, s[4:5] offset:592
	global_load_dwordx4 v[102:105], v118, s[4:5] offset:704
	global_load_dwordx4 v[110:113], v118, s[4:5] offset:720
	global_load_dwordx4 v[40:43], v[44:45], off offset:224
	global_load_dwordx4 v[82:85], v[44:45], off offset:256
	global_load_dwordx4 v[138:141], v[44:45], off offset:288
	global_load_dwordx4 v[70:73], v[44:45], off offset:320
	global_load_dwordx4 v[142:145], v[44:45], off offset:352
	v_mov_b32_e32 v31, s53
	s_mov_b32 m0, s71
	s_mov_b32 s12, 1
	s_waitcnt vmcnt(0)
	v_and_b32_e32 v191, 0xffff0000, v32
	v_lshlrev_b32_e32 v190, 16, v32
	v_lshlrev_b32_e32 v206, 16, v26
	v_and_b32_e32 v207, 0xffff0000, v26
	v_lshlrev_b32_e32 v208, 16, v27
	v_and_b32_e32 v209, 0xffff0000, v27
	v_lshlrev_b32_e32 v210, 16, v28
	v_and_b32_e32 v211, 0xffff0000, v28
	v_lshlrev_b32_e32 v212, 16, v29
	v_and_b32_e32 v213, 0xffff0000, v29
	v_lshlrev_b32_e32 v222, 16, v18
	v_and_b32_e32 v223, 0xffff0000, v18
	v_lshlrev_b32_e32 v224, 16, v19
	v_and_b32_e32 v225, 0xffff0000, v19
	v_lshlrev_b32_e32 v226, 16, v20
	v_and_b32_e32 v227, 0xffff0000, v20
	v_lshlrev_b32_e32 v228, 16, v21
	v_and_b32_e32 v229, 0xffff0000, v21
	global_load_dwordx4 v[26:29], v118, s[4:5] offset:640
	global_load_dwordx4 v[156:159], v118, s[4:5] offset:656
	global_load_dwordx4 v[18:21], v118, s[4:5] offset:528
	v_mul_f32_e32 v188, v191, v191
	v_lshlrev_b32_e32 v192, 16, v33
	v_fmac_f32_e32 v188, v190, v190
	v_and_b32_e32 v193, 0xffff0000, v33
	v_fmac_f32_e32 v188, v192, v192
	v_lshlrev_b32_e32 v194, 16, v34
	v_fmac_f32_e32 v188, v193, v193
	v_and_b32_e32 v195, 0xffff0000, v34
	v_fmac_f32_e32 v188, v194, v194
	v_lshlrev_b32_e32 v196, 16, v35
	v_fmac_f32_e32 v188, v195, v195
	v_and_b32_e32 v197, 0xffff0000, v35
	v_fmac_f32_e32 v188, v196, v196
	v_lshlrev_b32_e32 v198, 16, v36
	v_fmac_f32_e32 v188, v197, v197
	v_and_b32_e32 v199, 0xffff0000, v36
	v_fmac_f32_e32 v188, v198, v198
	v_lshlrev_b32_e32 v200, 16, v37
	v_lshlrev_b32_e32 v214, 16, v22
	v_and_b32_e32 v215, 0xffff0000, v22
	v_lshlrev_b32_e32 v216, 16, v23
	v_and_b32_e32 v217, 0xffff0000, v23
	v_lshlrev_b32_e32 v218, 16, v24
	v_and_b32_e32 v219, 0xffff0000, v24
	v_lshlrev_b32_e32 v220, 16, v25
	v_and_b32_e32 v221, 0xffff0000, v25
	v_fmac_f32_e32 v188, v199, v199
	global_load_dwordx4 v[22:25], v118, s[4:5] offset:512
	v_and_b32_e32 v201, 0xffff0000, v37
	v_fmac_f32_e32 v188, v200, v200
	v_lshlrev_b32_e32 v202, 16, v38
	v_fmac_f32_e32 v188, v201, v201
	v_and_b32_e32 v203, 0xffff0000, v38
	v_fmac_f32_e32 v188, v202, v202
	v_lshlrev_b32_e32 v204, 16, v39
	v_fmac_f32_e32 v188, v203, v203
	v_and_b32_e32 v205, 0xffff0000, v39
	v_fmac_f32_e32 v188, v204, v204
	v_fmac_f32_e32 v188, v205, v205
	v_fmac_f32_e32 v188, v206, v206
	v_fmac_f32_e32 v188, v207, v207
	v_fmac_f32_e32 v188, v208, v208
	v_fmac_f32_e32 v188, v209, v209
	v_fmac_f32_e32 v188, v210, v210
	v_fmac_f32_e32 v188, v211, v211
	v_fmac_f32_e32 v188, v212, v212
	v_fmac_f32_e32 v188, v213, v213
	v_fmac_f32_e32 v188, v214, v214
	v_fmac_f32_e32 v188, v215, v215
	v_fmac_f32_e32 v188, v216, v216
	v_fmac_f32_e32 v188, v217, v217
	v_fmac_f32_e32 v188, v218, v218
	v_fmac_f32_e32 v188, v219, v219
	v_fmac_f32_e32 v188, v220, v220
	v_fmac_f32_e32 v188, v221, v221
	v_fmac_f32_e32 v188, v222, v222
	v_fmac_f32_e32 v188, v223, v223
	v_fmac_f32_e32 v188, v224, v224
	v_fmac_f32_e32 v188, v225, v225
	v_fmac_f32_e32 v188, v226, v226
	v_fmac_f32_e32 v188, v227, v227
	v_fmac_f32_e32 v188, v228, v228
	v_lshlrev_b32_e32 v230, 16, v14
	v_fmac_f32_e32 v188, v229, v229
	v_and_b32_e32 v231, 0xffff0000, v14
	v_fmac_f32_e32 v188, v230, v230
	v_lshlrev_b32_e32 v232, 16, v15
	v_fmac_f32_e32 v188, v231, v231
	v_and_b32_e32 v233, 0xffff0000, v15
	v_fmac_f32_e32 v188, v232, v232
	v_lshlrev_b32_e32 v234, 16, v16
	v_fmac_f32_e32 v188, v233, v233
	v_and_b32_e32 v235, 0xffff0000, v16
	v_fmac_f32_e32 v188, v234, v234
	v_lshlrev_b32_e32 v246, 16, v40
	v_and_b32_e32 v247, 0xffff0000, v40
	v_lshlrev_b32_e32 v248, 16, v41
	v_and_b32_e32 v249, 0xffff0000, v41
	v_lshlrev_b32_e32 v250, 16, v42
	v_and_b32_e32 v251, 0xffff0000, v42
	v_lshlrev_b32_e32 v252, 16, v43
	v_and_b32_e32 v253, 0xffff0000, v43
	global_load_dwordx4 v[106:109], v118, s[4:5] offset:16
	global_load_dwordx4 v[114:117], v118, s[4:5]
	global_load_dwordx4 v[94:97], v118, s[4:5] offset:80
	global_load_dwordx4 v[98:101], v118, s[4:5] offset:64
	global_load_dwordx4 v[86:89], v118, s[4:5] offset:144
	global_load_dwordx4 v[90:93], v118, s[4:5] offset:128
	global_load_dwordx4 v[74:77], v118, s[4:5] offset:208
	global_load_dwordx4 v[78:81], v118, s[4:5] offset:192
	global_load_dwordx4 v[62:65], v118, s[4:5] offset:272
	global_load_dwordx4 v[66:69], v118, s[4:5] offset:256
	global_load_dwordx4 v[54:57], v118, s[4:5] offset:336
	global_load_dwordx4 v[58:61], v118, s[4:5] offset:320
	global_load_dwordx4 v[46:49], v118, s[4:5] offset:400
	global_load_dwordx4 v[50:53], v118, s[4:5] offset:384
	global_load_dwordx4 v[38:41], v118, s[4:5] offset:464
	global_load_dwordx4 v[42:45], v118, s[4:5] offset:448
	v_lshlrev_b32_e32 v236, 16, v17
	v_fmac_f32_e32 v188, v235, v235
	v_and_b32_e32 v237, 0xffff0000, v17
	v_fmac_f32_e32 v188, v236, v236
	v_lshlrev_b32_e32 v238, 16, v10
	v_fmac_f32_e32 v188, v237, v237
	v_and_b32_e32 v239, 0xffff0000, v10
	v_fmac_f32_e32 v188, v238, v238
	v_lshlrev_b32_e32 v240, 16, v11
	v_fmac_f32_e32 v188, v239, v239
	v_and_b32_e32 v241, 0xffff0000, v11
	v_fmac_f32_e32 v188, v240, v240
	v_lshlrev_b32_e32 v242, 16, v12
	v_fmac_f32_e32 v188, v241, v241
	v_and_b32_e32 v243, 0xffff0000, v12
	v_fmac_f32_e32 v188, v242, v242
	v_lshlrev_b32_e32 v244, 16, v13
	v_fmac_f32_e32 v188, v243, v243
	v_and_b32_e32 v245, 0xffff0000, v13
	v_fmac_f32_e32 v188, v244, v244
	v_fmac_f32_e32 v188, v245, v245
	v_fmac_f32_e32 v188, v246, v246
	v_fmac_f32_e32 v188, v247, v247
	v_fmac_f32_e32 v188, v248, v248
	v_fmac_f32_e32 v188, v249, v249
	v_fmac_f32_e32 v188, v250, v250
	v_fmac_f32_e32 v188, v251, v251
	v_fmac_f32_e32 v188, v252, v252
	v_lshlrev_b32_e32 v187, 16, v82
	v_lshlrev_b32_e32 v186, 16, v70
	v_fmac_f32_e32 v188, v253, v253
	v_lshlrev_b32_e32 v124, 16, v144
	v_and_b32_e32 v126, 0xffff0000, v144
	v_lshlrev_b32_e32 v131, 16, v139
	v_and_b32_e32 v133, 0xffff0000, v139
	v_lshlrev_b32_e32 v137, 16, v138
	v_lshlrev_b32_e32 v136, 16, v142
	v_and_b32_e32 v139, 0xffff0000, v138
	v_and_b32_e32 v138, 0xffff0000, v142
	v_lshlrev_b32_e32 v142, 16, v73
	v_and_b32_e32 v144, 0xffff0000, v73
	v_lshlrev_b32_e32 v152, 16, v72
	v_and_b32_e32 v154, 0xffff0000, v72
	v_pk_mul_f32 v[72:73], v[186:187], v[186:187]
	s_waitcnt vmcnt(18)
	v_mov_b32_e32 v150, v158
	v_mov_b32_e32 v158, v156
	v_lshlrev_b32_e32 v156, 16, v71
	v_and_b32_e32 v184, 0xffff0000, v71
	v_and_b32_e32 v189, 0xffff0000, v82
	v_add_f32_e32 v71, v73, v188
	v_and_b32_e32 v188, 0xffff0000, v70
	v_mov_b32_e32 v128, v110
	v_mov_b32_e32 v129, v2
	v_mov_b32_e32 v2, v111
	s_waitcnt vmcnt(17)
	v_mov_b32_e32 v151, v20
	v_mov_b32_e32 v20, v159
	v_mov_b32_e32 v159, v18
	v_mov_b32_e32 v18, v157
	v_lshlrev_b32_e32 v157, 16, v83
	v_pk_mul_f32 v[110:111], v[188:189], v[188:189]
	v_lshlrev_b32_e32 v119, 16, v141
	v_and_b32_e32 v121, 0xffff0000, v141
	v_lshlrev_b32_e32 v125, 16, v140
	v_and_b32_e32 v127, 0xffff0000, v140
	v_mov_b32_e32 v140, v102
	v_mov_b32_e32 v141, v6
	v_mov_b32_e32 v6, v103
	v_pk_mul_f32 v[102:103], v[156:157], v[156:157]
	v_and_b32_e32 v185, 0xffff0000, v83
	v_add_f32_e32 v70, v111, v71
	v_mov_b32_e32 v134, v104
	v_mov_b32_e32 v135, v8
	v_mov_b32_e32 v8, v105
	v_lshlrev_b32_e32 v153, 16, v84
	v_pk_mul_f32 v[104:105], v[184:185], v[184:185]
	v_add_f32_e32 v70, v103, v70
	v_pk_mul_f32 v[180:181], v[152:153], v[152:153]
	v_and_b32_e32 v155, 0xffff0000, v84
	v_add_f32_e32 v70, v105, v70
	v_lshlrev_b32_e32 v130, 16, v143
	v_and_b32_e32 v132, 0xffff0000, v143
	v_lshlrev_b32_e32 v143, 16, v85
	v_pk_mul_f32 v[182:183], v[154:155], v[154:155]
	v_add_f32_e32 v70, v181, v70
	v_lshlrev_b32_e32 v118, 16, v145
	v_and_b32_e32 v120, 0xffff0000, v145
	v_pk_mul_f32 v[176:177], v[142:143], v[142:143]
	v_and_b32_e32 v145, 0xffff0000, v85
	v_add_f32_e32 v70, v183, v70
	v_pk_mul_f32 v[178:179], v[144:145], v[144:145]
	v_add_f32_e32 v70, v177, v70
	v_pk_mul_f32 v[172:173], v[136:137], v[136:137]
	v_add_f32_e32 v70, v179, v70
	v_pk_mul_f32 v[174:175], v[138:139], v[138:139]
	v_add_f32_e32 v70, v173, v70
	v_add_f32_e32 v70, v175, v70
	v_fmac_f32_e32 v70, v131, v131
	v_fmac_f32_e32 v70, v133, v133
	v_fmac_f32_e32 v70, v125, v125
	v_fmac_f32_e32 v70, v127, v127
	v_fmac_f32_e32 v70, v119, v119
	v_fmac_f32_e32 v70, v121, v121
	v_add_f32_e32 v103, v72, v70
	v_add_f32_e32 v103, v110, v103
	v_add_f32_e32 v102, v102, v103
	v_add_f32_e32 v173, v104, v102
	v_add_f32_e32 v173, v180, v173
	v_add_f32_e32 v173, v182, v173
	v_add_f32_e32 v173, v176, v173
	v_add_f32_e32 v173, v178, v173
	v_mov_b32_e32 v176, v132
	v_mov_b32_e32 v177, v130
	s_waitcnt vmcnt(16)
	v_mov_b32_e32 v179, v24
	v_add_f32_e32 v24, v172, v173
	v_lshlrev_b64 v[10:11], 8, v[30:31]
	v_pk_mul_f32 v[176:177], v[176:177], v[176:177]
	v_add_f32_e32 v24, v174, v24
	v_lshl_add_u64 v[10:11], s[10:11], 0, v[10:11]
	v_lshlrev_b32_e32 v12, 6, v169
	v_mov_b32_e32 v13, v149
	v_mov_b32_e32 v180, v126
	v_mov_b32_e32 v181, v124
	v_add_f32_e32 v24, v177, v24
	v_lshl_add_u64 v[170:171], v[10:11], 0, v[12:13]
	v_pk_mul_f32 v[180:181], v[180:181], v[180:181]
	v_add_f32_e32 v24, v176, v24
	global_load_dwordx4 v[10:13], v[170:171], off offset:48
	global_load_dwordx4 v[14:17], v[170:171], off offset:32
	global_load_dwordx4 v[30:33], v[170:171], off offset:16
	global_load_dwordx4 v[34:37], v[170:171], off
	v_mov_b32_e32 v122, v112
	v_mov_b32_e32 v123, v4
	v_mov_b32_e32 v4, v113
	global_load_dwordx4 v[70:73], v[170:171], off offset:176
	global_load_dwordx4 v[82:85], v[170:171], off offset:160
	global_load_dwordx4 v[102:105], v[170:171], off offset:144
	global_load_dwordx4 v[110:113], v[170:171], off offset:128
	v_mov_b32_e32 v170, v120
	v_mov_b32_e32 v171, v118
	v_add_f32_e32 v24, v181, v24
	v_pk_mul_f32 v[170:171], v[170:171], v[170:171]
	v_add_f32_e32 v24, v180, v24
	v_add_f32_e32 v24, v171, v24
	v_add_f32_e32 v24, v170, v24
	v_mov_b32_e32 v178, v28
	v_mov_b32_e32 v28, v24
	s_nop 1
	v_permlane32_swap_b32_e32 v24, v28
	v_add_f32_e32 v24, v24, v28
	v_fmamk_f32 v24, v24, 0x3baaaaab, v163
	v_mul_f32_e32 v28, 0x4b800000, v24
	v_cmp_gt_f32_e32 vcc, s69, v24
	s_nop 1
	v_cndmask_b32_e32 v24, v24, v28, vcc
	v_rsq_f32_e32 v170, v24
	v_mov_b32_e32 v24, v29
	v_mov_b32_e32 v29, v22
	v_mov_b32_e32 v28, v26
	v_mul_f32_e32 v22, 0x45800000, v170
	v_cndmask_b32_e32 v22, v170, v22, vcc
	v_mul_f32_e32 v26, 0x3dd53b94, v22
	s_waitcnt vmcnt(22)
	v_mul_f32_e32 v22, v114, v26
	v_mul_f32_e32 v114, v22, v190
	v_mul_f32_e32 v22, v106, v26
	v_mul_f32_e32 v106, v22, v194
	v_mul_f32_e32 v22, v115, v26
	v_mul_f32_e32 v115, v22, v191
	v_mul_f32_e32 v22, v107, v26
	v_mul_f32_e32 v107, v22, v195
	v_mul_f32_e32 v22, v116, v26
	v_mul_f32_e32 v116, v22, v192
	v_mul_f32_e32 v22, v108, v26
	v_mul_f32_e32 v108, v22, v196
	v_mul_f32_e32 v22, v117, v26
	v_mul_f32_e32 v117, v22, v193
	v_mul_f32_e32 v22, v109, v26
	v_mul_f32_e32 v109, v22, v197
	s_waitcnt vmcnt(20)
	v_mul_f32_e32 v22, v98, v26
	v_mul_f32_e32 v170, v22, v198
	v_mul_f32_e32 v22, v94, v26
	v_mul_f32_e32 v94, v22, v202
	v_mul_f32_e32 v22, v99, v26
	v_mul_f32_e32 v171, v22, v199
	v_mul_f32_e32 v22, v95, v26
	v_mul_f32_e32 v95, v22, v203
	v_mul_f32_e32 v22, v100, v26
	v_mul_f32_e32 v172, v22, v200
	v_mul_f32_e32 v22, v96, v26
	v_mul_f32_e32 v96, v22, v204
	v_mul_f32_e32 v22, v101, v26
	v_mul_f32_e32 v173, v22, v201
	v_mul_f32_e32 v22, v97, v26
	v_mul_f32_e32 v97, v22, v205
	s_waitcnt vmcnt(18)
	v_mul_f32_e32 v22, v90, v26
	v_mul_f32_e32 v90, v22, v206
	v_mul_f32_e32 v22, v86, v26
	v_mul_f32_e32 v86, v22, v210
	v_mul_f32_e32 v22, v91, v26
	v_mul_f32_e32 v91, v22, v207
	v_mul_f32_e32 v22, v87, v26
	v_mul_f32_e32 v87, v22, v211
	v_mul_f32_e32 v22, v92, v26
	v_mul_f32_e32 v92, v22, v208
	v_mul_f32_e32 v22, v88, v26
	v_mul_f32_e32 v88, v22, v212
	v_mul_f32_e32 v22, v93, v26
	v_mul_f32_e32 v93, v22, v209
	v_mul_f32_e32 v22, v89, v26
	v_mul_f32_e32 v89, v22, v213
	s_waitcnt vmcnt(16)
	v_mul_f32_e32 v22, v78, v26
	v_mul_f32_e32 v78, v22, v214
	v_mul_f32_e32 v22, v74, v26
	v_mul_f32_e32 v74, v22, v218
	v_mul_f32_e32 v22, v79, v26
	v_mul_f32_e32 v79, v22, v215
	v_mul_f32_e32 v22, v75, v26
	v_mul_f32_e32 v75, v22, v219
	v_mul_f32_e32 v22, v80, v26
	v_mul_f32_e32 v80, v22, v216
	v_mul_f32_e32 v22, v76, v26
	v_mul_f32_e32 v76, v22, v220
	v_mul_f32_e32 v22, v81, v26
	v_mul_f32_e32 v81, v22, v217
	v_mul_f32_e32 v22, v77, v26
	v_mul_f32_e32 v77, v22, v221
	s_waitcnt vmcnt(14)
	v_mul_f32_e32 v22, v66, v26
	v_mul_f32_e32 v66, v22, v222
	v_mul_f32_e32 v22, v26, v62
	v_mul_f32_e32 v62, v22, v226
	v_mul_f32_e32 v22, v67, v26
	v_mul_f32_e32 v67, v22, v223
	v_mul_f32_e32 v22, v26, v63
	v_mul_f32_e32 v63, v22, v227
	v_mul_f32_e32 v22, v68, v26
	v_mul_f32_e32 v68, v22, v224
	v_mul_f32_e32 v22, v26, v64
	v_mul_f32_e32 v64, v22, v228
	v_mul_f32_e32 v22, v69, v26
	v_mul_f32_e32 v69, v22, v225
	v_mul_f32_e32 v22, v26, v65
	v_mul_f32_e32 v65, v22, v229
	s_waitcnt vmcnt(12)
	v_mul_f32_e32 v22, v26, v58
	v_mul_f32_e32 v58, v22, v230
	v_mul_f32_e32 v22, v26, v54
	v_mul_f32_e32 v54, v22, v234
	v_mul_f32_e32 v22, v26, v59
	v_mul_f32_e32 v59, v22, v231
	v_mul_f32_e32 v22, v26, v55
	v_mul_f32_e32 v55, v22, v235
	v_mul_f32_e32 v22, v26, v60
	v_mul_f32_e32 v60, v22, v232
	v_mul_f32_e32 v22, v26, v56
	v_mul_f32_e32 v56, v22, v236
	v_mul_f32_e32 v22, v26, v61
	v_mul_f32_e32 v61, v22, v233
	v_mul_f32_e32 v22, v26, v57
	v_mul_f32_e32 v57, v22, v237
	s_waitcnt vmcnt(10)
	v_mul_f32_e32 v22, v26, v50
	v_mul_f32_e32 v174, v22, v238
	v_mul_f32_e32 v22, v26, v46
	v_mul_f32_e32 v175, v22, v242
	v_mul_f32_e32 v22, v26, v51
	v_mul_f32_e32 v176, v22, v239
	v_mul_f32_e32 v22, v26, v47
	v_mul_f32_e32 v177, v22, v243
	v_mul_f32_e32 v22, v26, v52
	v_mul_f32_e32 v52, v22, v240
	v_mul_f32_e32 v22, v26, v48
	v_mul_f32_e32 v180, v22, v244
	v_mul_f32_e32 v22, v26, v53
	v_mul_f32_e32 v53, v22, v241
	v_mul_f32_e32 v22, v26, v49
	v_mul_f32_e32 v181, v22, v245
	s_waitcnt vmcnt(8)
	v_mul_f32_e32 v22, v26, v42
	v_mul_f32_e32 v182, v22, v246
	v_mul_f32_e32 v22, v26, v38
	v_mul_f32_e32 v183, v22, v250
	v_mul_f32_e32 v22, v26, v43
	v_mul_f32_e32 v190, v22, v247
	v_mul_f32_e32 v22, v26, v39
	v_mul_f32_e32 v191, v22, v251
	v_mul_f32_e32 v22, v26, v44
	v_mul_f32_e32 v192, v22, v248
	v_mul_f32_e32 v22, v26, v40
	v_mul_f32_e32 v193, v22, v252
	v_mul_f32_e32 v22, v26, v45
	v_mul_f32_e32 v194, v22, v249
	v_mul_f32_e32 v22, v26, v41
	v_pk_mul_f32 v[28:29], v[26:27], v[28:29] op_sel_hi:[0,1]
	v_mul_f32_e32 v195, v22, v253
	v_pk_mul_f32 v[28:29], v[28:29], v[186:187]
	v_mov_b32_e32 v22, v27
	v_pk_mul_f32 v[38:39], v[26:27], v[158:159] op_sel_hi:[0,1]
	v_pk_mul_f32 v[22:23], v[26:27], v[22:23] op_sel_hi:[0,1]
	v_pk_mul_f32 v[18:19], v[26:27], v[18:19] op_sel_hi:[0,1]
	v_pk_mul_f32 v[40:41], v[26:27], v[178:179] op_sel_hi:[0,1]
	v_pk_mul_f32 v[42:43], v[26:27], v[150:151] op_sel_hi:[0,1]
	v_pk_mul_f32 v[24:25], v[26:27], v[24:25] op_sel_hi:[0,1]
	v_pk_mul_f32 v[20:21], v[26:27], v[20:21] op_sel_hi:[0,1]
	v_pk_mul_f32 v[44:45], v[26:27], v[140:141] op_sel_hi:[0,1]
	v_pk_mul_f32 v[46:47], v[26:27], v[128:129] op_sel_hi:[0,1]
	v_pk_mul_f32 v[6:7], v[26:27], v[6:7] op_sel_hi:[0,1]
	v_pk_mul_f32 v[2:3], v[26:27], v[2:3] op_sel_hi:[0,1]
	v_pk_mul_f32 v[48:49], v[26:27], v[134:135] op_sel_hi:[0,1]
	v_pk_mul_f32 v[50:51], v[26:27], v[122:123] op_sel_hi:[0,1]
	v_pk_mul_f32 v[8:9], v[26:27], v[8:9] op_sel_hi:[0,1]
	v_pk_mul_f32 v[4:5], v[26:27], v[4:5] op_sel_hi:[0,1]
	s_waitcnt vmcnt(4)
	v_pk_mul_f32 v[26:27], v[28:29], v[34:35] op_sel:[1,0] op_sel_hi:[0,1]
	v_pk_mul_f32 v[22:23], v[22:23], v[188:189]
	v_pk_mul_f32 v[48:49], v[48:49], v[130:131]
	v_sub_f32_e32 v130, v26, v27
	v_pk_mul_f32 v[26:27], v[28:29], v[34:35]
	v_pk_mul_f32 v[40:41], v[40:41], v[156:157]
	v_add_f32_e32 v28, v27, v26
	v_pk_mul_f32 v[26:27], v[22:23], v[36:37] op_sel:[1,0] op_sel_hi:[0,1]
	v_pk_mul_f32 v[22:23], v[22:23], v[36:37]
	v_sub_f32_e32 v26, v26, v27
	v_add_f32_e32 v27, v23, v22
	v_pk_mul_f32 v[22:23], v[40:41], v[30:31] op_sel:[1,0] op_sel_hi:[0,1]
	v_pk_mul_f32 v[24:25], v[24:25], v[184:185]
	v_sub_f32_e32 v29, v22, v23
	v_pk_mul_f32 v[22:23], v[40:41], v[30:31]
	v_pk_mul_f32 v[38:39], v[38:39], v[152:153]
	v_add_f32_e32 v30, v23, v22
	v_pk_mul_f32 v[22:23], v[24:25], v[32:33] op_sel:[1,0] op_sel_hi:[0,1]
	v_sub_f32_e32 v31, v22, v23
	v_pk_mul_f32 v[22:23], v[24:25], v[32:33]
	v_pk_mul_f32 v[18:19], v[18:19], v[154:155]
	v_add_f32_e32 v24, v23, v22
	v_pk_mul_f32 v[22:23], v[38:39], v[14:15] op_sel:[1,0] op_sel_hi:[0,1]
	v_pk_mul_f32 v[14:15], v[38:39], v[14:15]
	v_sub_f32_e32 v22, v22, v23
	v_add_f32_e32 v23, v15, v14
	v_pk_mul_f32 v[14:15], v[18:19], v[16:17] op_sel:[1,0] op_sel_hi:[0,1]
	v_pk_mul_f32 v[42:43], v[42:43], v[142:143]
	v_sub_f32_e32 v25, v14, v15
	v_pk_mul_f32 v[14:15], v[18:19], v[16:17]
	v_pk_mul_f32 v[20:21], v[20:21], v[144:145]
	v_add_f32_e32 v16, v15, v14
	v_pk_mul_f32 v[14:15], v[42:43], v[10:11] op_sel:[1,0] op_sel_hi:[0,1]
	v_pk_mul_f32 v[10:11], v[42:43], v[10:11]
	v_sub_f32_e32 v14, v14, v15
	v_add_f32_e32 v15, v11, v10
	v_pk_mul_f32 v[10:11], v[20:21], v[12:13] op_sel:[1,0] op_sel_hi:[0,1]
	v_pk_mul_f32 v[44:45], v[44:45], v[136:137]
	v_sub_f32_e32 v17, v10, v11
	v_pk_mul_f32 v[10:11], v[20:21], v[12:13]
	v_pk_mul_f32 v[6:7], v[6:7], v[138:139]
	v_add_f32_e32 v12, v11, v10
	s_waitcnt vmcnt(0)
	v_pk_mul_f32 v[10:11], v[44:45], v[110:111] op_sel:[1,0] op_sel_hi:[0,1]
	v_sub_f32_e32 v13, v10, v11
	v_pk_mul_f32 v[10:11], v[44:45], v[110:111]
	v_pk_mul_f32 v[8:9], v[8:9], v[132:133]
	v_add_f32_e32 v18, v11, v10
	v_pk_mul_f32 v[10:11], v[6:7], v[112:113] op_sel:[1,0] op_sel_hi:[0,1]
	v_pk_mul_f32 v[6:7], v[6:7], v[112:113]
	v_sub_f32_e32 v10, v10, v11
	v_add_f32_e32 v11, v7, v6
	v_pk_mul_f32 v[6:7], v[48:49], v[102:103] op_sel:[1,0] op_sel_hi:[0,1]
	v_sub_f32_e32 v19, v6, v7
	v_pk_mul_f32 v[6:7], v[48:49], v[102:103]
	v_pk_mul_f32 v[46:47], v[46:47], v[124:125]
	v_add_f32_e32 v20, v7, v6
	v_pk_mul_f32 v[6:7], v[8:9], v[104:105] op_sel:[1,0] op_sel_hi:[0,1]
	v_sub_f32_e32 v21, v6, v7
	v_pk_mul_f32 v[6:7], v[8:9], v[104:105]
	v_pk_mul_f32 v[2:3], v[2:3], v[126:127]
	v_add_f32_e32 v8, v7, v6
	v_pk_mul_f32 v[6:7], v[46:47], v[82:83] op_sel:[1,0] op_sel_hi:[0,1]
	v_sub_f32_e32 v9, v6, v7
	v_pk_mul_f32 v[6:7], v[46:47], v[82:83]
	v_pk_mul_f32 v[50:51], v[50:51], v[118:119]
	v_add_f32_e32 v32, v7, v6
	v_pk_mul_f32 v[6:7], v[2:3], v[84:85] op_sel:[1,0] op_sel_hi:[0,1]
	v_pk_mul_f32 v[2:3], v[2:3], v[84:85]
	v_sub_f32_e32 v6, v6, v7
	v_add_f32_e32 v7, v3, v2
	v_pk_mul_f32 v[2:3], v[50:51], v[70:71] op_sel:[1,0] op_sel_hi:[0,1]
	v_pk_mul_f32 v[4:5], v[4:5], v[120:121]
	v_sub_f32_e32 v33, v2, v3
	v_pk_mul_f32 v[2:3], v[50:51], v[70:71]
	v_cvt_pk_bf16_f32 v98, v114, v115
	v_cvt_pk_bf16_f32 v99, v116, v117
	v_cvt_pk_bf16_f32 v100, v106, v107
	v_cvt_pk_bf16_f32 v101, v108, v109
	v_cvt_pk_bf16_f32 v102, v170, v171
	s_nop 0
	v_add_f32_e32 v34, v3, v2
	v_pk_mul_f32 v[2:3], v[4:5], v[72:73] op_sel:[1,0] op_sel_hi:[0,1]
	v_sub_f32_e32 v35, v2, v3
	v_pk_mul_f32 v[2:3], v[4:5], v[72:73]
	v_cvt_pk_bf16_f32 v103, v172, v173
	v_cvt_pk_bf16_f32 v104, v94, v95
	v_cvt_pk_bf16_f32 v105, v96, v97
	v_cvt_pk_bf16_f32 v106, v90, v91
	v_cvt_pk_bf16_f32 v107, v92, v93
	s_nop 0
	v_add_f32_e32 v2, v3, v2
	v_cvt_pk_bf16_f32 v108, v86, v87
	v_cvt_pk_bf16_f32 v109, v88, v89
	v_cvt_pk_bf16_f32 v110, v78, v79
	v_cvt_pk_bf16_f32 v111, v80, v81
	v_cvt_pk_bf16_f32 v112, v74, v75
	v_cvt_pk_bf16_f32 v113, v76, v77
	v_cvt_pk_bf16_f32 v114, v66, v67
	v_cvt_pk_bf16_f32 v115, v68, v69
	v_cvt_pk_bf16_f32 v116, v62, v63
	v_cvt_pk_bf16_f32 v117, v64, v65
	v_cvt_pk_bf16_f32 v118, v58, v59
	v_cvt_pk_bf16_f32 v119, v60, v61
	v_cvt_pk_bf16_f32 v120, v54, v55
	v_cvt_pk_bf16_f32 v121, v56, v57
	v_cvt_pk_bf16_f32 v122, v174, v176
	v_cvt_pk_bf16_f32 v123, v52, v53
	v_cvt_pk_bf16_f32 v124, v175, v177
	v_cvt_pk_bf16_f32 v125, v180, v181
	v_cvt_pk_bf16_f32 v126, v182, v190
	v_cvt_pk_bf16_f32 v127, v192, v194
	v_cvt_pk_bf16_f32 v128, v183, v191
	v_cvt_pk_bf16_f32 v129, v193, v195
	v_cvt_pk_bf16_f32 v130, v130, v26
	v_cvt_pk_bf16_f32 v131, v29, v31
	v_cvt_pk_bf16_f32 v132, v22, v25
	v_cvt_pk_bf16_f32 v133, v14, v17
	v_cvt_pk_bf16_f32 v134, v13, v10
	v_cvt_pk_bf16_f32 v135, v19, v21
	v_cvt_pk_bf16_f32 v136, v9, v6
	v_cvt_pk_bf16_f32 v137, v33, v35
	v_cvt_pk_bf16_f32 v138, v28, v27
	v_cvt_pk_bf16_f32 v139, v30, v24
	v_cvt_pk_bf16_f32 v140, v23, v16
	v_cvt_pk_bf16_f32 v141, v15, v12
	v_cvt_pk_bf16_f32 v142, v18, v11
	v_cvt_pk_bf16_f32 v143, v20, v8
	v_cvt_pk_bf16_f32 v144, v32, v7
	v_cvt_pk_bf16_f32 v145, v34, v2
	v_mul_hi_i32 v2, v168, s70
	v_lshrrev_b32_e32 v3, 31, v2
	v_ashrrev_i32_e32 v2, 2, v2
	v_add_u32_e32 v2, v2, v3
	v_mul_lo_u32 v3, v2, 24
	v_sub_u32_e32 v3, v168, v3
	v_bitop3_b32 v3, v2, v3, 7 bitop3:0x6c
	v_mul_lo_u32 v2, v2, s68
	v_lshl_add_u32 v2, v3, 4, v2
	v_add_u32_e32 v3, 0x200, v168
	v_mul_hi_i32 v4, v3, s70
	v_lshrrev_b32_e32 v5, 31, v4
	v_ashrrev_i32_e32 v4, 2, v4
	v_add_u32_e32 v4, v4, v5
	v_mul_lo_u32 v5, v4, 24
	v_sub_u32_e32 v5, v3, v5
	v_bitop3_b32 v5, v4, v5, 7 bitop3:0x6c
	v_mul_lo_u32 v4, v4, s68
	v_lshl_add_u32 v4, v5, 4, v4
	v_add_u32_e32 v5, 0x400, v168
	v_mul_hi_i32 v6, v5, s70
	v_lshrrev_b32_e32 v7, 31, v6
	v_ashrrev_i32_e32 v6, 2, v6
	v_add_u32_e32 v6, v6, v7
	v_mul_lo_u32 v7, v6, 24
	v_sub_u32_e32 v5, v5, v7
	v_bitop3_b32 v5, v6, v5, 7 bitop3:0x6c
	v_mul_lo_u32 v6, v6, s68
	v_ashrrev_i32_e32 v9, 4, v168
	v_lshl_add_u32 v6, v5, 4, v6
	v_bfe_u32 v5, v168, 2, 2
	v_lshrrev_b32_e32 v7, 1, v168
	v_and_b32_e32 v10, 0x1ffff0, v9
	v_lshrrev_b32_e32 v9, 1, v9
	v_ashrrev_i32_e32 v3, 4, v3
	v_and_or_b32 v5, v7, 8, v5
	v_and_b32_e32 v7, 0x60, v168
	v_lshlrev_b32_e32 v8, 3, v168
	v_and_b32_e32 v9, 4, v9
	v_and_b32_e32 v11, 0x1ffff0, v3
	v_lshrrev_b32_e32 v3, 1, v3
	v_and_or_b32 v7, v8, 24, v7
	v_or3_b32 v9, v10, v9, v5
	v_and_b32_e32 v3, 4, v3
	s_barrier
	global_load_lds_dwordx4 v2, s[44:45]
	s_mov_b32 m0, s72
	v_lshlrev_b32_e32 v7, 1, v7
	v_lshlrev_b32_e32 v10, 11, v9
	v_or3_b32 v3, v11, v3, v5
	global_load_lds_dwordx4 v4, s[44:45]
	s_mov_b32 m0, s73
	v_or_b32_e32 v9, v10, v7
	v_lshlrev_b32_e32 v11, 11, v3
	global_load_lds_dwordx4 v6, s[44:45]
	s_mov_b32 m0, s64
	v_or_b32_e32 v3, v11, v7
	global_load_lds_dwordx4 v9, s[46:47]
	s_mov_b32 m0, s74
	v_lshlrev_b32_e32 v13, 1, v168
	global_load_lds_dwordx4 v3, s[46:47]
	v_lshlrev_b32_e32 v9, 4, v168
	v_and_b32_e32 v14, 32, v13
	v_or_b32_e32 v3, 32, v148
	v_mul_u32_u24_e32 v5, 0x180, v167
	v_and_b32_e32 v7, 0x70, v9
	v_and_b32_e32 v12, 0xc0, v9
	v_and_or_b32 v8, v8, s75, v14
	v_bitop3_b32 v172, v3, v5, v7 bitop3:0xde
	v_or_b32_e32 v3, 64, v148
	v_mul_i32_i24_e32 v15, -4, v169
	v_add3_u32 v169, v12, 0, v8
	v_and_b32_e32 v12, 0xc0, v13
	v_and_b32_e32 v13, 48, v9
	v_bitop3_b32 v173, v3, v5, v7 bitop3:0xde
	v_or_b32_e32 v3, 0x60, v148
	v_or3_b32 v8, v11, v12, v13
	v_mov_b32_e32 v9, v149
	v_bitop3_b32 v171, v148, v5, v7 bitop3:0xde
	v_bitop3_b32 v174, v3, v5, v7 bitop3:0xde
	v_mov_b32_e32 v3, v149
	v_mov_b32_e32 v5, v149
	v_mov_b32_e32 v7, v149
	v_lshl_add_u64 v[150:151], s[48:49], 0, v[8:9]
	v_or3_b32 v8, v10, v12, v13
	v_mov_b32_e32 v16, v149
	v_mov_b32_e32 v17, v149
	v_and_b32_e32 v170, 63, v168
	s_lshl_b32 s46, s80, 2
	v_lshl_add_u32 v168, v167, 2, s65
	v_lshl_add_u64 v[152:153], s[48:49], 0, v[8:9]
	v_lshl_add_u64 v[154:155], s[50:51], 0, v[6:7]
	v_lshl_add_u64 v[156:157], s[50:51], 0, v[4:5]
	v_lshl_add_u64 v[158:159], s[50:51], 0, v[2:3]
	v_add3_u32 v167, s63, v15, v167
	v_mov_b32_e32 v2, v149
	v_mov_b32_e32 v4, v149
	v_mov_b32_e32 v6, v149
	v_mov_b32_e32 v8, v149
	v_mov_b32_e32 v10, v149
	v_mov_b32_e32 v11, v149
	v_mov_b32_e32 v12, v149
	v_mov_b32_e32 v13, v149
	v_mov_b32_e32 v14, v149
	v_mov_b32_e32 v15, v149
	v_mov_b64_e32 v[32:33], v[16:17]
	v_mov_b64_e32 v[48:49], v[16:17]
	v_mov_b64_e32 v[64:65], v[16:17]
	s_add_i32 s46, s46, 4
	v_cmp_gt_u32_e64 s[0:1], 32, v170
	v_mov_b32_e32 v176, 0
	v_mov_b32_e32 v175, 0xf149f2ca
	s_movk_i32 s47, 0xff00
	v_mov_b64_e32 v[30:31], v[14:15]
	v_mov_b64_e32 v[28:29], v[12:13]
	v_mov_b64_e32 v[26:27], v[10:11]
	v_mov_b64_e32 v[24:25], v[8:9]
	v_mov_b64_e32 v[22:23], v[6:7]
	v_mov_b64_e32 v[20:21], v[4:5]
	v_mov_b64_e32 v[18:19], v[2:3]
	v_mov_b64_e32 v[46:47], v[14:15]
	v_mov_b64_e32 v[44:45], v[12:13]
	v_mov_b64_e32 v[42:43], v[10:11]
	v_mov_b64_e32 v[40:41], v[8:9]
	v_mov_b64_e32 v[38:39], v[6:7]
	v_mov_b64_e32 v[36:37], v[4:5]
	v_mov_b64_e32 v[34:35], v[2:3]
	v_mov_b64_e32 v[62:63], v[14:15]
	v_mov_b64_e32 v[60:61], v[12:13]
	v_mov_b64_e32 v[58:59], v[10:11]
	v_mov_b64_e32 v[56:57], v[8:9]
	v_mov_b64_e32 v[54:55], v[6:7]
	v_mov_b64_e32 v[52:53], v[4:5]
	v_mov_b64_e32 v[50:51], v[2:3]

.LBB0_1840:
	s_add_i32 s74, s73, 0x80
	s_and_b64 s[30:31], s[10:11], exec
	s_cselect_b32 s31, 0, s74
	s_add_i32 s74, s74, s70
	s_or_b32 s30, s31, 0x80
	s_waitcnt lgkmcnt(8)
	s_barrier
	s_waitcnt lgkmcnt(0)
	s_and_b64 s[10:11], s[10:11], exec
	s_cselect_b32 s10, s71, s74
	s_add_i32 s11, s10, 0x80
	s_setprio 1
	s_waitcnt lgkmcnt(0)
	v_mfma_scale_f32_16x16x128_f8f6f4 v[170:173], v[2:9], v[42:49], v[170:173], v193, v193 op_sel_hi:[0,0,0]
	v_mfma_scale_f32_16x16x128_f8f6f4 v[162:165], v[10:17], v[42:49], v[162:165], v193, v193 op_sel_hi:[0,0,0]
	v_mfma_scale_f32_16x16x128_f8f6f4 v[154:157], v[2:9], v[34:41], v[154:157], v193, v193 op_sel_hi:[0,0,0]
	v_mfma_scale_f32_16x16x128_f8f6f4 v[146:149], v[10:17], v[34:41], v[146:149], v193, v193 op_sel_hi:[0,0,0]
	v_mfma_scale_f32_16x16x128_f8f6f4 v[138:141], v[2:9], v[26:33], v[138:141], v193, v193 op_sel_hi:[0,0,0]
	v_mfma_scale_f32_16x16x128_f8f6f4 v[130:133], v[10:17], v[26:33], v[130:133], v193, v193 op_sel_hi:[0,0,0]
	v_mfma_scale_f32_16x16x128_f8f6f4 v[122:125], v[2:9], v[18:25], v[122:125], v193, v193 op_sel_hi:[0,0,0]
	v_mfma_scale_f32_16x16x128_f8f6f4 v[114:117], v[10:17], v[18:25], v[114:117], v193, v193 op_sel_hi:[0,0,0]
	s_setprio 0
	s_barrier
	v_add_u32_e32 v216, s59, v189
	ds_read_b128 v[204:207], v216
	ds_read_b128 v[208:211], v216 offset:1024
	ds_read_b128 v[212:215], v216 offset:2048
	ds_read_b128 v[216:219], v216 offset:3072
	s_barrier
	s_waitcnt lgkmcnt(0)
	s_setprio 1
	s_waitcnt lgkmcnt(0)
	v_mfma_scale_f32_16x16x128_f8f6f4 v[174:177], v[204:211], v[42:49], v[174:177], v193, v193 op_sel_hi:[0,0,0]
	v_mfma_scale_f32_16x16x128_f8f6f4 v[166:169], v[212:219], v[42:49], v[166:169], v193, v193 op_sel_hi:[0,0,0]
	s_mov_b32 m0, s38
	v_add_u32_e32 v220, s10, v181
	global_load_lds_dwordx4 v220, s[20:21]
	v_mfma_scale_f32_16x16x128_f8f6f4 v[158:161], v[204:211], v[34:41], v[158:161], v193, v193 op_sel_hi:[0,0,0]
	v_mfma_scale_f32_16x16x128_f8f6f4 v[150:153], v[212:219], v[34:41], v[150:153], v193, v193 op_sel_hi:[0,0,0]
	v_mfma_scale_f32_16x16x128_f8f6f4 v[142:145], v[204:211], v[26:33], v[142:145], v193, v193 op_sel_hi:[0,0,0]
	v_add_u32_e32 v220, s10, v182
	s_mov_b32 m0, s39
	s_nop 0
	global_load_lds_dwordx4 v220, s[20:21]
	v_mfma_scale_f32_16x16x128_f8f6f4 v[134:137], v[212:219], v[26:33], v[134:137], v193, v193 op_sel_hi:[0,0,0]
	v_mfma_scale_f32_16x16x128_f8f6f4 v[126:129], v[204:211], v[18:25], v[126:129], v193, v193 op_sel_hi:[0,0,0]
	v_mfma_scale_f32_16x16x128_f8f6f4 v[118:121], v[212:219], v[18:25], v[118:121], v193, v193 op_sel_hi:[0,0,0]
	s_setprio 0
	s_barrier
	ds_read_b128 v[18:21], v194 offset:16384
	ds_read_b128 v[22:25], v194 offset:17408
	ds_read_b128 v[26:29], v194 offset:18432
	ds_read_b128 v[30:33], v194 offset:19456
	ds_read_b128 v[34:37], v194 offset:20480
	ds_read_b128 v[38:41], v194 offset:21504
	ds_read_b128 v[42:45], v194 offset:22528
	ds_read_b128 v[46:49], v194 offset:23552
	s_barrier
	s_waitcnt lgkmcnt(0)
	s_setprio 1
	s_waitcnt lgkmcnt(0)
	v_mfma_scale_f32_16x16x128_f8f6f4 v[110:113], v[2:9], v[18:25], v[110:113], v193, v193 op_sel_hi:[0,0,0]
	v_mfma_scale_f32_16x16x128_f8f6f4 v[102:105], v[10:17], v[18:25], v[102:105], v193, v193 op_sel_hi:[0,0,0]
	s_mov_b32 m0, s37
	v_add_u32_e32 v220, s31, v183
	global_load_lds_dwordx4 v220, s[18:19]
	v_mfma_scale_f32_16x16x128_f8f6f4 v[94:97], v[2:9], v[26:33], v[94:97], v193, v193 op_sel_hi:[0,0,0]
	v_mfma_scale_f32_16x16x128_f8f6f4 v[86:89], v[10:17], v[26:33], v[86:89], v193, v193 op_sel_hi:[0,0,0]
	v_mfma_scale_f32_16x16x128_f8f6f4 v[78:81], v[2:9], v[34:41], v[78:81], v193, v193 op_sel_hi:[0,0,0]
	v_add_u32_e32 v220, s31, v184
	s_mov_b32 m0, s40
	s_nop 0
	global_load_lds_dwordx4 v220, s[18:19]
	v_mfma_scale_f32_16x16x128_f8f6f4 v[70:73], v[10:17], v[34:41], v[70:73], v193, v193 op_sel_hi:[0,0,0]
	v_mfma_scale_f32_16x16x128_f8f6f4 v[62:65], v[2:9], v[42:49], v[62:65], v193, v193 op_sel_hi:[0,0,0]
	v_mfma_scale_f32_16x16x128_f8f6f4 v[54:57], v[10:17], v[42:49], v[54:57], v193, v193 op_sel_hi:[0,0,0]
	s_setprio 0
	s_barrier
	s_add_i32 s74, s10, 0x40000
	s_add_i32 s75, s59, s36
	s_waitcnt vmcnt(4)
	s_barrier
	s_setprio 1
	v_mfma_scale_f32_16x16x128_f8f6f4 v[106:109], v[204:211], v[18:25], v[106:109], v193, v193 op_sel_hi:[0,0,0]
	v_mfma_scale_f32_16x16x128_f8f6f4 v[98:101], v[212:219], v[18:25], v[98:101], v193, v193 op_sel_hi:[0,0,0]
	v_add_u32_e32 v2, s74, v181
	s_mov_b32 m0, s75
	s_nop 0
	global_load_lds_dwordx4 v2, s[20:21]
	v_mfma_scale_f32_16x16x128_f8f6f4 v[90:93], v[204:211], v[26:33], v[90:93], v193, v193 op_sel_hi:[0,0,0]
	v_mfma_scale_f32_16x16x128_f8f6f4 v[82:85], v[212:219], v[26:33], v[82:85], v193, v193 op_sel_hi:[0,0,0]
	v_mfma_scale_f32_16x16x128_f8f6f4 v[74:77], v[204:211], v[34:41], v[74:77], v193, v193 op_sel_hi:[0,0,0]
	v_add_u32_e32 v2, s74, v182
	s_add_i32 m0, s75, 0x2000
	s_nop 0
	global_load_lds_dwordx4 v2, s[20:21]
	v_mfma_scale_f32_16x16x128_f8f6f4 v[66:69], v[212:219], v[34:41], v[66:69], v193, v193 op_sel_hi:[0,0,0]
	v_mfma_scale_f32_16x16x128_f8f6f4 v[58:61], v[204:211], v[42:49], v[58:61], v193, v193 op_sel_hi:[0,0,0]
	v_mfma_scale_f32_16x16x128_f8f6f4 v[50:53], v[212:219], v[42:49], v[50:53], v193, v193 op_sel_hi:[0,0,0]
	s_setprio 0
	s_add_i32 s74, 0, 0x18000
	v_add_u32_e32 v14, s74, v189
	s_barrier
	ds_read_b128 v[2:5], v14
	ds_read_b128 v[6:9], v14 offset:1024
	ds_read_b128 v[10:13], v14 offset:2048
	ds_read_b128 v[14:17], v14 offset:3072
	ds_read_b128 v[18:21], v194 offset:32768
	ds_read_b128 v[22:25], v194 offset:33792
	ds_read_b128 v[26:29], v194 offset:34816
	ds_read_b128 v[30:33], v194 offset:35840
	ds_read_b128 v[34:37], v194 offset:36864
	ds_read_b128 v[38:41], v194 offset:37888
	ds_read_b128 v[42:45], v194 offset:38912
	ds_read_b128 v[46:49], v194 offset:39936
	s_waitcnt lgkmcnt(8)
	s_barrier
	s_waitcnt lgkmcnt(0)
	s_setprio 1
	s_waitcnt lgkmcnt(0)
	v_mfma_scale_f32_16x16x128_f8f6f4 v[170:173], v[2:9], v[18:25], v[170:173], v193, v193 op_sel_hi:[0,0,0]
	v_mfma_scale_f32_16x16x128_f8f6f4 v[162:165], v[10:17], v[18:25], v[162:165], v193, v193 op_sel_hi:[0,0,0]
	s_mov_b32 m0, s41
	v_add_u32_e32 v204, s31, v185
	global_load_lds_dwordx4 v204, s[18:19]
	v_mfma_scale_f32_16x16x128_f8f6f4 v[154:157], v[2:9], v[26:33], v[154:157], v193, v193 op_sel_hi:[0,0,0]
	v_mfma_scale_f32_16x16x128_f8f6f4 v[146:149], v[10:17], v[26:33], v[146:149], v193, v193 op_sel_hi:[0,0,0]
	v_mfma_scale_f32_16x16x128_f8f6f4 v[138:141], v[2:9], v[34:41], v[138:141], v193, v193 op_sel_hi:[0,0,0]
	v_add_u32_e32 v204, s31, v186
	s_mov_b32 m0, s42
	s_nop 0
	global_load_lds_dwordx4 v204, s[18:19]
	v_mfma_scale_f32_16x16x128_f8f6f4 v[130:133], v[10:17], v[34:41], v[130:133], v193, v193 op_sel_hi:[0,0,0]
	v_mfma_scale_f32_16x16x128_f8f6f4 v[122:125], v[2:9], v[42:49], v[122:125], v193, v193 op_sel_hi:[0,0,0]
	v_mfma_scale_f32_16x16x128_f8f6f4 v[114:117], v[10:17], v[42:49], v[114:117], v193, v193 op_sel_hi:[0,0,0]
	s_setprio 0
	s_barrier
	s_add_i32 s31, 0, 0x1c000
	s_add_i32 s74, s74, s36
	v_add_u32_e32 v216, s31, v189
	ds_read_b128 v[204:207], v216
	ds_read_b128 v[208:211], v216 offset:1024
	ds_read_b128 v[212:215], v216 offset:2048
	ds_read_b128 v[216:219], v216 offset:3072
	s_barrier
	s_waitcnt lgkmcnt(0)
	s_setprio 1
	s_waitcnt lgkmcnt(0)
	v_mfma_scale_f32_16x16x128_f8f6f4 v[174:177], v[204:211], v[18:25], v[174:177], v193, v193 op_sel_hi:[0,0,0]
	v_mfma_scale_f32_16x16x128_f8f6f4 v[166:169], v[212:219], v[18:25], v[166:169], v193, v193 op_sel_hi:[0,0,0]
	v_add_u32_e32 v220, s11, v181
	s_mov_b32 m0, s74
	global_load_lds_dwordx4 v220, s[20:21]
	v_mfma_scale_f32_16x16x128_f8f6f4 v[158:161], v[204:211], v[26:33], v[158:161], v193, v193 op_sel_hi:[0,0,0]
	v_mfma_scale_f32_16x16x128_f8f6f4 v[150:153], v[212:219], v[26:33], v[150:153], v193, v193 op_sel_hi:[0,0,0]
	v_mfma_scale_f32_16x16x128_f8f6f4 v[142:145], v[204:211], v[34:41], v[142:145], v193, v193 op_sel_hi:[0,0,0]
	v_add_u32_e32 v220, s11, v182
	s_add_i32 m0, s74, 0x2000
	s_nop 0
	global_load_lds_dwordx4 v220, s[20:21]
	v_mfma_scale_f32_16x16x128_f8f6f4 v[134:137], v[212:219], v[34:41], v[134:137], v193, v193 op_sel_hi:[0,0,0]
	v_mfma_scale_f32_16x16x128_f8f6f4 v[126:129], v[204:211], v[42:49], v[126:129], v193, v193 op_sel_hi:[0,0,0]
	v_mfma_scale_f32_16x16x128_f8f6f4 v[118:121], v[212:219], v[42:49], v[118:121], v193, v193 op_sel_hi:[0,0,0]
	s_setprio 0
	s_barrier
	ds_read_b128 v[18:21], v194 offset:49152
	ds_read_b128 v[22:25], v194 offset:50176
	ds_read_b128 v[26:29], v194 offset:51200
	ds_read_b128 v[30:33], v194 offset:52224
	ds_read_b128 v[34:37], v194 offset:53248
	ds_read_b128 v[38:41], v194 offset:54272
	ds_read_b128 v[42:45], v194 offset:55296
	ds_read_b128 v[46:49], v194 offset:56320
	s_barrier
	s_waitcnt lgkmcnt(0)
	s_setprio 1
	s_waitcnt lgkmcnt(0)
	v_mfma_scale_f32_16x16x128_f8f6f4 v[110:113], v[2:9], v[18:25], v[110:113], v193, v193 op_sel_hi:[0,0,0]
	v_mfma_scale_f32_16x16x128_f8f6f4 v[102:105], v[10:17], v[18:25], v[102:105], v193, v193 op_sel_hi:[0,0,0]
	s_mov_b32 m0, s49
	v_add_u32_e32 v220, s30, v183
	global_load_lds_dwordx4 v220, s[18:19]
	v_mfma_scale_f32_16x16x128_f8f6f4 v[94:97], v[2:9], v[26:33], v[94:97], v193, v193 op_sel_hi:[0,0,0]
	v_mfma_scale_f32_16x16x128_f8f6f4 v[86:89], v[10:17], v[26:33], v[86:89], v193, v193 op_sel_hi:[0,0,0]
	v_mfma_scale_f32_16x16x128_f8f6f4 v[78:81], v[2:9], v[34:41], v[78:81], v193, v193 op_sel_hi:[0,0,0]
	v_add_u32_e32 v220, s30, v184
	s_mov_b32 m0, s50
	s_nop 0
	global_load_lds_dwordx4 v220, s[18:19]
	v_mfma_scale_f32_16x16x128_f8f6f4 v[70:73], v[10:17], v[34:41], v[70:73], v193, v193 op_sel_hi:[0,0,0]
	v_mfma_scale_f32_16x16x128_f8f6f4 v[62:65], v[2:9], v[42:49], v[62:65], v193, v193 op_sel_hi:[0,0,0]
	v_mfma_scale_f32_16x16x128_f8f6f4 v[54:57], v[10:17], v[42:49], v[54:57], v193, v193 op_sel_hi:[0,0,0]
	s_setprio 0
	s_barrier
	s_add_i32 s10, s10, 0x40080
	s_add_i32 s11, s31, s36
	s_waitcnt vmcnt(4)
	s_barrier
	s_setprio 1
	v_mfma_scale_f32_16x16x128_f8f6f4 v[106:109], v[204:211], v[18:25], v[106:109], v193, v193 op_sel_hi:[0,0,0]
	v_mfma_scale_f32_16x16x128_f8f6f4 v[98:101], v[212:219], v[18:25], v[98:101], v193, v193 op_sel_hi:[0,0,0]
	v_add_u32_e32 v2, s10, v181
	s_mov_b32 m0, s11
	s_nop 0
	global_load_lds_dwordx4 v2, s[20:21]
	v_mfma_scale_f32_16x16x128_f8f6f4 v[90:93], v[204:211], v[26:33], v[90:93], v193, v193 op_sel_hi:[0,0,0]
	v_mfma_scale_f32_16x16x128_f8f6f4 v[82:85], v[212:219], v[26:33], v[82:85], v193, v193 op_sel_hi:[0,0,0]
	v_mfma_scale_f32_16x16x128_f8f6f4 v[74:77], v[204:211], v[34:41], v[74:77], v193, v193 op_sel_hi:[0,0,0]
	v_add_u32_e32 v2, s10, v182
	s_add_i32 m0, s11, 0x2000
	s_nop 0
	global_load_lds_dwordx4 v2, s[20:21]
	v_mfma_scale_f32_16x16x128_f8f6f4 v[66:69], v[212:219], v[34:41], v[66:69], v193, v193 op_sel_hi:[0,0,0]
	v_mfma_scale_f32_16x16x128_f8f6f4 v[58:61], v[204:211], v[42:49], v[58:61], v193, v193 op_sel_hi:[0,0,0]
	v_mfma_scale_f32_16x16x128_f8f6f4 v[50:53], v[212:219], v[42:49], v[50:53], v193, v193 op_sel_hi:[0,0,0]
	s_setprio 0
	s_add_i32 s72, s72, 2
	s_addk_i32 s73, 0x100
	s_cmp_ge_i32 s72, s51
	s_barrier
	s_cbranch_scc1 .LBB0_1830
